# static priority raise for waves 4-7 now persists through the GEMM epilogues (reset only at the phase seams) instead of being reset after every k-loop
# baseline (speedup 1.0000x reference)
.Lprio_P2a:
.LBB0_418:
	ds_read_b128 v[148:151], v168
	ds_read_b128 v[152:155], v168 offset:1024
	ds_read_b128 v[172:175], v168 offset:2048
	ds_read_b128 v[176:179], v168 offset:3072
	ds_read_b128 v[186:189], v169
	ds_read_b128 v[190:193], v169 offset:1024
	ds_read_b128 v[194:197], v169 offset:2048
	ds_read_b128 v[198:201], v169 offset:3072
	s_add_u32 s38, s34, 0xfff00080
	s_addc_u32 s39, s35, -1
	s_cmp_eq_u32 s67, 60
	s_cselect_b32 s45, s5, s39
	s_cselect_b32 s44, s7, s38
	s_cselect_b32 s43, s15, s66
	s_cselect_b32 s42, s25, s63
	s_add_i32 m0, s46, 0xc000
	ds_read_b128 v[202:205], v170
	ds_read_b128 v[206:209], v170 offset:1024
	ds_read_b128 v[210:213], v170 offset:2048
	ds_read_b128 v[214:217], v170 offset:3072
	ds_read_b128 v[218:221], v170 offset:4096
	ds_read_b128 v[222:225], v170 offset:5120
	ds_read_b128 v[226:229], v170 offset:6144
	ds_read_b128 v[230:233], v170 offset:7168
	global_load_lds_dwordx4 v140, s[34:35]
	s_add_i32 m0, s46, 0xe000
	s_nop 0
	global_load_lds_dwordx4 v142, s[34:35]
	s_waitcnt vmcnt(8)
	s_waitcnt lgkmcnt(0)
	s_barrier
	s_waitcnt lgkmcnt(0)
	v_mfma_f32_16x16x32_f16 v[126:129], v[148:151], v[202:205], v[126:129]
	v_mfma_f32_16x16x32_f16 v[122:125], v[172:175], v[202:205], v[122:125]
	v_mfma_f32_16x16x32_f16 v[110:113], v[148:151], v[210:213], v[110:113]
	v_mfma_f32_16x16x32_f16 v[106:109], v[172:175], v[210:213], v[106:109]
	v_mfma_f32_16x16x32_f16 v[94:97], v[148:151], v[218:221], v[94:97]
	v_mfma_f32_16x16x32_f16 v[90:93], v[172:175], v[218:221], v[90:93]
	v_mfma_f32_16x16x32_f16 v[78:81], v[148:151], v[226:229], v[78:81]
	v_mfma_f32_16x16x32_f16 v[74:77], v[172:175], v[226:229], v[74:77]
	v_mfma_f32_16x16x32_f16 v[126:129], v[152:155], v[206:209], v[126:129]
	v_mfma_f32_16x16x32_f16 v[122:125], v[176:179], v[206:209], v[122:125]
	v_mfma_f32_16x16x32_f16 v[110:113], v[152:155], v[214:217], v[110:113]
	v_mfma_f32_16x16x32_f16 v[106:109], v[176:179], v[214:217], v[106:109]
	v_mfma_f32_16x16x32_f16 v[94:97], v[152:155], v[222:225], v[94:97]
	v_mfma_f32_16x16x32_f16 v[90:93], v[176:179], v[222:225], v[90:93]
	v_mfma_f32_16x16x32_f16 v[78:81], v[152:155], v[230:233], v[78:81]
	v_mfma_f32_16x16x32_f16 v[74:77], v[176:179], v[230:233], v[74:77]
	v_mfma_f32_16x16x32_f16 v[118:121], v[186:189], v[202:205], v[118:121]
	v_mfma_f32_16x16x32_f16 v[114:117], v[194:197], v[202:205], v[114:117]
	v_mfma_f32_16x16x32_f16 v[102:105], v[186:189], v[210:213], v[102:105]
	v_mfma_f32_16x16x32_f16 v[98:101], v[194:197], v[210:213], v[98:101]
	v_mfma_f32_16x16x32_f16 v[86:89], v[186:189], v[218:221], v[86:89]
	v_mfma_f32_16x16x32_f16 v[82:85], v[194:197], v[218:221], v[82:85]
	v_mfma_f32_16x16x32_f16 v[70:73], v[186:189], v[226:229], v[70:73]
	v_mfma_f32_16x16x32_f16 v[66:69], v[194:197], v[226:229], v[66:69]
	v_mfma_f32_16x16x32_f16 v[118:121], v[190:193], v[206:209], v[118:121]
	v_mfma_f32_16x16x32_f16 v[114:117], v[198:201], v[206:209], v[114:117]
	v_mfma_f32_16x16x32_f16 v[102:105], v[190:193], v[214:217], v[102:105]
	v_mfma_f32_16x16x32_f16 v[98:101], v[198:201], v[214:217], v[98:101]
	v_mfma_f32_16x16x32_f16 v[86:89], v[190:193], v[222:225], v[86:89]
	v_mfma_f32_16x16x32_f16 v[82:85], v[198:201], v[222:225], v[82:85]
	v_mfma_f32_16x16x32_f16 v[70:73], v[190:193], v[230:233], v[70:73]
	v_mfma_f32_16x16x32_f16 v[66:69], v[198:201], v[230:233], v[66:69]
	s_barrier
	s_add_u32 s98, s42, s10
	s_addc_u32 s99, s43, s11
	s_add_u32 s100, s44, s10
	s_addc_u32 s101, s45, s11
	s_add_i32 s38, s61, s33
	s_mov_b32 m0, s38
	ds_read_b128 v[202:205], v170 offset:16384
	ds_read_b128 v[206:209], v170 offset:17408
	ds_read_b128 v[210:213], v170 offset:18432
	ds_read_b128 v[214:217], v170 offset:19456
	ds_read_b128 v[218:221], v170 offset:20480
	ds_read_b128 v[222:225], v170 offset:21504
	ds_read_b128 v[226:229], v170 offset:22528
	ds_read_b128 v[230:233], v170 offset:23552
	global_load_lds_dwordx4 v132, s[42:43]
	s_add_i32 m0, s38, 0x2000
	s_add_u32 s72, s42, 0x100000
	s_addc_u32 s73, s43, 0
	s_add_i32 s38, s62, s33
	global_load_lds_dwordx4 v136, s[42:43]
	s_mov_b32 m0, s38
	s_nop 0
	global_load_lds_dwordx4 v132, s[72:73]
	s_add_i32 m0, s38, 0x2000
	s_nop 0
	global_load_lds_dwordx4 v136, s[72:73]
	s_mov_b32 m0, s46
	s_nop 0
	global_load_lds_dwordx4 v130, s[44:45]
	s_mov_b32 m0, s47
	s_nop 0
	global_load_lds_dwordx4 v134, s[44:45]
	s_waitcnt vmcnt(8)
	s_waitcnt lgkmcnt(0)
	s_barrier
	s_waitcnt lgkmcnt(0)
	v_mfma_f32_16x16x32_f16 v[62:65], v[148:151], v[202:205], v[62:65]
	v_mfma_f32_16x16x32_f16 v[58:61], v[172:175], v[202:205], v[58:61]
	v_mfma_f32_16x16x32_f16 v[46:49], v[148:151], v[210:213], v[46:49]
	v_mfma_f32_16x16x32_f16 v[42:45], v[172:175], v[210:213], v[42:45]
	v_mfma_f32_16x16x32_f16 v[30:33], v[148:151], v[218:221], v[30:33]
	v_mfma_f32_16x16x32_f16 v[26:29], v[172:175], v[218:221], v[26:29]
	v_mfma_f32_16x16x32_f16 v[14:17], v[148:151], v[226:229], v[14:17]
	v_mfma_f32_16x16x32_f16 v[10:13], v[172:175], v[226:229], v[10:13]
	v_mfma_f32_16x16x32_f16 v[62:65], v[152:155], v[206:209], v[62:65]
	v_mfma_f32_16x16x32_f16 v[58:61], v[176:179], v[206:209], v[58:61]
	v_mfma_f32_16x16x32_f16 v[46:49], v[152:155], v[214:217], v[46:49]
	v_mfma_f32_16x16x32_f16 v[42:45], v[176:179], v[214:217], v[42:45]
	v_mfma_f32_16x16x32_f16 v[30:33], v[152:155], v[222:225], v[30:33]
	v_mfma_f32_16x16x32_f16 v[26:29], v[176:179], v[222:225], v[26:29]
	v_mfma_f32_16x16x32_f16 v[14:17], v[152:155], v[230:233], v[14:17]
	v_mfma_f32_16x16x32_f16 v[10:13], v[176:179], v[230:233], v[10:13]
	v_mfma_f32_16x16x32_f16 v[54:57], v[186:189], v[202:205], v[54:57]
	v_mfma_f32_16x16x32_f16 v[50:53], v[194:197], v[202:205], v[50:53]
	v_mfma_f32_16x16x32_f16 v[38:41], v[186:189], v[210:213], v[38:41]
	v_mfma_f32_16x16x32_f16 v[34:37], v[194:197], v[210:213], v[34:37]
	v_mfma_f32_16x16x32_f16 v[22:25], v[186:189], v[218:221], v[22:25]
	v_mfma_f32_16x16x32_f16 v[18:21], v[194:197], v[218:221], v[18:21]
	v_mfma_f32_16x16x32_f16 v[6:9], v[186:189], v[226:229], v[6:9]
	v_mfma_f32_16x16x32_f16 v[2:5], v[194:197], v[226:229], v[2:5]
	v_mfma_f32_16x16x32_f16 v[54:57], v[190:193], v[206:209], v[54:57]
	v_mfma_f32_16x16x32_f16 v[50:53], v[198:201], v[206:209], v[50:53]
	v_mfma_f32_16x16x32_f16 v[38:41], v[190:193], v[214:217], v[38:41]
	v_mfma_f32_16x16x32_f16 v[34:37], v[198:201], v[214:217], v[34:37]
	v_mfma_f32_16x16x32_f16 v[22:25], v[190:193], v[222:225], v[22:25]
	v_mfma_f32_16x16x32_f16 v[18:21], v[198:201], v[222:225], v[18:21]
	v_mfma_f32_16x16x32_f16 v[6:9], v[190:193], v[230:233], v[6:9]
	v_mfma_f32_16x16x32_f16 v[2:5], v[198:201], v[230:233], v[2:5]
	s_barrier
	s_add_i32 s38, 0, 0x18000
	v_add_u32_e32 v138, s38, v164
	s_add_i32 s39, 0, 0x1c000
	ds_read_b128 v[148:151], v138
	ds_read_b128 v[152:155], v138 offset:1024
	ds_read_b128 v[172:175], v138 offset:2048
	ds_read_b128 v[176:179], v138 offset:3072
	v_add_u32_e32 v138, s39, v164
	ds_read_b128 v[186:189], v138
	ds_read_b128 v[190:193], v138 offset:1024
	ds_read_b128 v[194:197], v138 offset:2048
	ds_read_b128 v[198:201], v138 offset:3072
	s_add_u32 s44, s44, 0x100000
	s_addc_u32 s45, s45, 0
	s_mov_b32 m0, s50
	ds_read_b128 v[202:205], v170 offset:32768
	ds_read_b128 v[206:209], v170 offset:33792
	ds_read_b128 v[210:213], v170 offset:34816
	ds_read_b128 v[214:217], v170 offset:35840
	ds_read_b128 v[218:221], v170 offset:36864
	ds_read_b128 v[222:225], v170 offset:37888
	ds_read_b128 v[226:229], v170 offset:38912
	ds_read_b128 v[230:233], v170 offset:39936
	global_load_lds_dwordx4 v130, s[44:45]
	s_mov_b32 m0, s51
	s_nop 0
	global_load_lds_dwordx4 v134, s[44:45]
	s_waitcnt vmcnt(8)
	s_waitcnt lgkmcnt(0)
	s_barrier
	s_waitcnt lgkmcnt(0)
	v_mfma_f32_16x16x32_f16 v[126:129], v[148:151], v[202:205], v[126:129]
	v_mfma_f32_16x16x32_f16 v[122:125], v[172:175], v[202:205], v[122:125]
	v_mfma_f32_16x16x32_f16 v[110:113], v[148:151], v[210:213], v[110:113]
	v_mfma_f32_16x16x32_f16 v[106:109], v[172:175], v[210:213], v[106:109]
	v_mfma_f32_16x16x32_f16 v[94:97], v[148:151], v[218:221], v[94:97]
	v_mfma_f32_16x16x32_f16 v[90:93], v[172:175], v[218:221], v[90:93]
	v_mfma_f32_16x16x32_f16 v[78:81], v[148:151], v[226:229], v[78:81]
	v_mfma_f32_16x16x32_f16 v[74:77], v[172:175], v[226:229], v[74:77]
	v_mfma_f32_16x16x32_f16 v[126:129], v[152:155], v[206:209], v[126:129]
	v_mfma_f32_16x16x32_f16 v[122:125], v[176:179], v[206:209], v[122:125]
	v_mfma_f32_16x16x32_f16 v[110:113], v[152:155], v[214:217], v[110:113]
	v_mfma_f32_16x16x32_f16 v[106:109], v[176:179], v[214:217], v[106:109]
	v_mfma_f32_16x16x32_f16 v[94:97], v[152:155], v[222:225], v[94:97]
	v_mfma_f32_16x16x32_f16 v[90:93], v[176:179], v[222:225], v[90:93]
	v_mfma_f32_16x16x32_f16 v[78:81], v[152:155], v[230:233], v[78:81]
	v_mfma_f32_16x16x32_f16 v[74:77], v[176:179], v[230:233], v[74:77]
	v_mfma_f32_16x16x32_f16 v[118:121], v[186:189], v[202:205], v[118:121]
	v_mfma_f32_16x16x32_f16 v[114:117], v[194:197], v[202:205], v[114:117]
	v_mfma_f32_16x16x32_f16 v[102:105], v[186:189], v[210:213], v[102:105]
	v_mfma_f32_16x16x32_f16 v[98:101], v[194:197], v[210:213], v[98:101]
	v_mfma_f32_16x16x32_f16 v[86:89], v[186:189], v[218:221], v[86:89]
	v_mfma_f32_16x16x32_f16 v[82:85], v[194:197], v[218:221], v[82:85]
	v_mfma_f32_16x16x32_f16 v[70:73], v[186:189], v[226:229], v[70:73]
	v_mfma_f32_16x16x32_f16 v[66:69], v[194:197], v[226:229], v[66:69]
	v_mfma_f32_16x16x32_f16 v[118:121], v[190:193], v[206:209], v[118:121]
	v_mfma_f32_16x16x32_f16 v[114:117], v[198:201], v[206:209], v[114:117]
	v_mfma_f32_16x16x32_f16 v[102:105], v[190:193], v[214:217], v[102:105]
	v_mfma_f32_16x16x32_f16 v[98:101], v[198:201], v[214:217], v[98:101]
	v_mfma_f32_16x16x32_f16 v[86:89], v[190:193], v[222:225], v[86:89]
	v_mfma_f32_16x16x32_f16 v[82:85], v[198:201], v[222:225], v[82:85]
	v_mfma_f32_16x16x32_f16 v[70:73], v[190:193], v[230:233], v[70:73]
	v_mfma_f32_16x16x32_f16 v[66:69], v[198:201], v[230:233], v[66:69]
	s_barrier
	s_add_i32 s38, s38, s33
	s_mov_b32 m0, s38
	ds_read_b128 v[202:205], v170 offset:49152
	ds_read_b128 v[206:209], v170 offset:50176
	ds_read_b128 v[210:213], v170 offset:51200
	ds_read_b128 v[214:217], v170 offset:52224
	ds_read_b128 v[218:221], v170 offset:53248
	ds_read_b128 v[222:225], v170 offset:54272
	ds_read_b128 v[226:229], v170 offset:55296
	ds_read_b128 v[230:233], v170 offset:56320
	global_load_lds_dwordx4 v132, s[98:99]
	s_add_i32 m0, s38, 0x2000
	s_add_u32 s42, s42, 0x100080
	s_addc_u32 s43, s43, 0
	s_add_i32 s38, s39, s33
	global_load_lds_dwordx4 v136, s[98:99]
	s_mov_b32 m0, s38
	s_nop 0
	global_load_lds_dwordx4 v132, s[42:43]
	s_add_i32 m0, s38, 0x2000
	s_nop 0
	global_load_lds_dwordx4 v136, s[42:43]
	s_mov_b32 m0, s53
	s_nop 0
	global_load_lds_dwordx4 v130, s[100:101]
	s_mov_b32 m0, s58
	s_nop 0
	global_load_lds_dwordx4 v134, s[100:101]
	s_waitcnt vmcnt(8)
	s_waitcnt lgkmcnt(0)
	s_barrier
	s_waitcnt lgkmcnt(0)
	v_mfma_f32_16x16x32_f16 v[62:65], v[148:151], v[202:205], v[62:65]
	v_mfma_f32_16x16x32_f16 v[58:61], v[172:175], v[202:205], v[58:61]
	v_mfma_f32_16x16x32_f16 v[46:49], v[148:151], v[210:213], v[46:49]
	v_mfma_f32_16x16x32_f16 v[42:45], v[172:175], v[210:213], v[42:45]
	v_mfma_f32_16x16x32_f16 v[30:33], v[148:151], v[218:221], v[30:33]
	v_mfma_f32_16x16x32_f16 v[26:29], v[172:175], v[218:221], v[26:29]
	v_mfma_f32_16x16x32_f16 v[14:17], v[148:151], v[226:229], v[14:17]
	v_mfma_f32_16x16x32_f16 v[10:13], v[172:175], v[226:229], v[10:13]
	v_mfma_f32_16x16x32_f16 v[62:65], v[152:155], v[206:209], v[62:65]
	v_mfma_f32_16x16x32_f16 v[58:61], v[176:179], v[206:209], v[58:61]
	v_mfma_f32_16x16x32_f16 v[46:49], v[152:155], v[214:217], v[46:49]
	v_mfma_f32_16x16x32_f16 v[42:45], v[176:179], v[214:217], v[42:45]
	v_mfma_f32_16x16x32_f16 v[30:33], v[152:155], v[222:225], v[30:33]
	v_mfma_f32_16x16x32_f16 v[26:29], v[176:179], v[222:225], v[26:29]
	v_mfma_f32_16x16x32_f16 v[14:17], v[152:155], v[230:233], v[14:17]
	v_mfma_f32_16x16x32_f16 v[10:13], v[176:179], v[230:233], v[10:13]
	v_mfma_f32_16x16x32_f16 v[54:57], v[186:189], v[202:205], v[54:57]
	v_mfma_f32_16x16x32_f16 v[50:53], v[194:197], v[202:205], v[50:53]
	v_mfma_f32_16x16x32_f16 v[38:41], v[186:189], v[210:213], v[38:41]
	v_mfma_f32_16x16x32_f16 v[34:37], v[194:197], v[210:213], v[34:37]
	v_mfma_f32_16x16x32_f16 v[22:25], v[186:189], v[218:221], v[22:25]
	v_mfma_f32_16x16x32_f16 v[18:21], v[194:197], v[218:221], v[18:21]
	v_mfma_f32_16x16x32_f16 v[6:9], v[186:189], v[226:229], v[6:9]
	v_mfma_f32_16x16x32_f16 v[2:5], v[194:197], v[226:229], v[2:5]
	v_mfma_f32_16x16x32_f16 v[54:57], v[190:193], v[206:209], v[54:57]
	v_mfma_f32_16x16x32_f16 v[50:53], v[198:201], v[206:209], v[50:53]
	v_mfma_f32_16x16x32_f16 v[38:41], v[190:193], v[214:217], v[38:41]
	v_mfma_f32_16x16x32_f16 v[34:37], v[198:201], v[214:217], v[34:37]
	v_mfma_f32_16x16x32_f16 v[22:25], v[190:193], v[222:225], v[22:25]
	v_mfma_f32_16x16x32_f16 v[18:21], v[198:201], v[222:225], v[18:21]
	v_mfma_f32_16x16x32_f16 v[6:9], v[190:193], v[230:233], v[6:9]
	v_mfma_f32_16x16x32_f16 v[2:5], v[198:201], v[230:233], v[2:5]
	s_barrier
	s_add_i32 s67, s67, 2
	s_add_u32 s34, s34, 0x100
	s_addc_u32 s35, s35, 0
	s_add_u32 s63, s63, 0x100
	s_addc_u32 s66, s66, 0
	s_cmp_gt_u32 s67, 61
	s_cbranch_scc0 .LBB0_418
	s_and_b64 vcc, exec, s[12:13]
	s_cbranch_vccz .LBB0_421
	s_barrier

.Lprio_P2b:
.LBB0_547:
	ds_read_b128 v[26:29], v191
	ds_read_b128 v[30:33], v191 offset:1024
	ds_read_b128 v[42:45], v191 offset:2048
	ds_read_b128 v[46:49], v191 offset:3072
	ds_read_b128 v[168:171], v192
	ds_read_b128 v[172:175], v192 offset:1024
	ds_read_b128 v[176:179], v192 offset:2048
	ds_read_b128 v[194:197], v192 offset:3072
	s_add_u32 s38, s34, 0xfff80080
	s_addc_u32 s39, s35, -1
	s_cmp_eq_u32 s74, 28
	s_cselect_b32 s45, s5, s39
	s_cselect_b32 s44, s7, s38
	s_cselect_b32 s43, s8, s73
	s_cselect_b32 s42, s65, s67
	s_add_i32 m0, s50, 0xc000
	ds_read_b128 v[198:201], v193
	ds_read_b128 v[202:205], v193 offset:1024
	ds_read_b128 v[206:209], v193 offset:2048
	ds_read_b128 v[210:213], v193 offset:3072
	ds_read_b128 v[214:217], v193 offset:4096
	ds_read_b128 v[218:221], v193 offset:5120
	ds_read_b128 v[222:225], v193 offset:6144
	ds_read_b128 v[226:229], v193 offset:7168
	global_load_lds_dwordx4 v156, s[34:35]
	s_add_i32 m0, s50, 0xe000
	s_nop 0
	global_load_lds_dwordx4 v158, s[34:35]
	s_waitcnt vmcnt(8)
	s_waitcnt lgkmcnt(0)
	s_barrier
	s_waitcnt lgkmcnt(0)
	v_mfma_i32_16x16x64_i8 v[142:145], v[26:29], v[198:201], v[142:145]
	v_mfma_i32_16x16x64_i8 v[138:141], v[42:45], v[198:201], v[138:141]
	v_mfma_i32_16x16x64_i8 v[126:129], v[26:29], v[206:209], v[126:129]
	v_mfma_i32_16x16x64_i8 v[122:125], v[42:45], v[206:209], v[122:125]
	v_mfma_i32_16x16x64_i8 v[110:113], v[26:29], v[214:217], v[110:113]
	v_mfma_i32_16x16x64_i8 v[106:109], v[42:45], v[214:217], v[106:109]
	v_mfma_i32_16x16x64_i8 v[94:97], v[26:29], v[222:225], v[94:97]
	v_mfma_i32_16x16x64_i8 v[90:93], v[42:45], v[222:225], v[90:93]
	v_mfma_i32_16x16x64_i8 v[142:145], v[30:33], v[202:205], v[142:145]
	v_mfma_i32_16x16x64_i8 v[138:141], v[46:49], v[202:205], v[138:141]
	v_mfma_i32_16x16x64_i8 v[126:129], v[30:33], v[210:213], v[126:129]
	v_mfma_i32_16x16x64_i8 v[122:125], v[46:49], v[210:213], v[122:125]
	v_mfma_i32_16x16x64_i8 v[110:113], v[30:33], v[218:221], v[110:113]
	v_mfma_i32_16x16x64_i8 v[106:109], v[46:49], v[218:221], v[106:109]
	v_mfma_i32_16x16x64_i8 v[94:97], v[30:33], v[226:229], v[94:97]
	v_mfma_i32_16x16x64_i8 v[90:93], v[46:49], v[226:229], v[90:93]
	v_mfma_i32_16x16x64_i8 v[134:137], v[168:171], v[198:201], v[134:137]
	v_mfma_i32_16x16x64_i8 v[130:133], v[176:179], v[198:201], v[130:133]
	v_mfma_i32_16x16x64_i8 v[118:121], v[168:171], v[206:209], v[118:121]
	v_mfma_i32_16x16x64_i8 v[114:117], v[176:179], v[206:209], v[114:117]
	v_mfma_i32_16x16x64_i8 v[102:105], v[168:171], v[214:217], v[102:105]
	v_mfma_i32_16x16x64_i8 v[98:101], v[176:179], v[214:217], v[98:101]
	v_mfma_i32_16x16x64_i8 v[86:89], v[168:171], v[222:225], v[86:89]
	v_mfma_i32_16x16x64_i8 v[82:85], v[176:179], v[222:225], v[82:85]
	v_mfma_i32_16x16x64_i8 v[134:137], v[172:175], v[202:205], v[134:137]
	v_mfma_i32_16x16x64_i8 v[130:133], v[194:197], v[202:205], v[130:133]
	v_mfma_i32_16x16x64_i8 v[118:121], v[172:175], v[210:213], v[118:121]
	v_mfma_i32_16x16x64_i8 v[114:117], v[194:197], v[210:213], v[114:117]
	v_mfma_i32_16x16x64_i8 v[102:105], v[172:175], v[218:221], v[102:105]
	v_mfma_i32_16x16x64_i8 v[98:101], v[194:197], v[218:221], v[98:101]
	v_mfma_i32_16x16x64_i8 v[86:89], v[172:175], v[226:229], v[86:89]
	v_mfma_i32_16x16x64_i8 v[82:85], v[194:197], v[226:229], v[82:85]
	s_barrier
	s_add_u32 s98, s42, s12
	s_addc_u32 s99, s43, s13
	s_add_u32 s100, s44, s12
	s_addc_u32 s101, s45, s13
	s_add_i32 s38, s62, s47
	s_mov_b32 m0, s38
	ds_read_b128 v[198:201], v193 offset:16384
	ds_read_b128 v[202:205], v193 offset:17408
	ds_read_b128 v[206:209], v193 offset:18432
	ds_read_b128 v[210:213], v193 offset:19456
	ds_read_b128 v[214:217], v193 offset:20480
	ds_read_b128 v[218:221], v193 offset:21504
	ds_read_b128 v[222:225], v193 offset:22528
	ds_read_b128 v[226:229], v193 offset:23552
	global_load_lds_dwordx4 v148, s[42:43]
	s_add_i32 m0, s38, 0x2000
	s_add_u32 s76, s42, 0x80000
	s_addc_u32 s77, s43, 0
	s_add_i32 s38, s63, s47
	global_load_lds_dwordx4 v152, s[42:43]
	s_mov_b32 m0, s38
	s_nop 0
	global_load_lds_dwordx4 v148, s[76:77]
	s_add_i32 m0, s38, 0x2000
	s_nop 0
	global_load_lds_dwordx4 v152, s[76:77]
	s_mov_b32 m0, s50
	s_nop 0
	global_load_lds_dwordx4 v146, s[44:45]
	s_mov_b32 m0, s51
	s_nop 0
	global_load_lds_dwordx4 v150, s[44:45]
	s_waitcnt vmcnt(8)
	s_waitcnt lgkmcnt(0)
	s_barrier
	s_waitcnt lgkmcnt(0)
	v_mfma_i32_16x16x64_i8 v[78:81], v[26:29], v[198:201], v[78:81]
	v_mfma_i32_16x16x64_i8 v[74:77], v[42:45], v[198:201], v[74:77]
	v_mfma_i32_16x16x64_i8 v[62:65], v[26:29], v[206:209], v[62:65]
	v_mfma_i32_16x16x64_i8 v[58:61], v[42:45], v[206:209], v[58:61]
	v_mfma_i32_16x16x64_i8 v[38:41], v[26:29], v[214:217], v[38:41]
	v_mfma_i32_16x16x64_i8 v[34:37], v[42:45], v[214:217], v[34:37]
	v_mfma_i32_16x16x64_i8 v[14:17], v[26:29], v[222:225], v[14:17]
	v_mfma_i32_16x16x64_i8 v[10:13], v[42:45], v[222:225], v[10:13]
	v_mfma_i32_16x16x64_i8 v[78:81], v[30:33], v[202:205], v[78:81]
	v_mfma_i32_16x16x64_i8 v[74:77], v[46:49], v[202:205], v[74:77]
	v_mfma_i32_16x16x64_i8 v[62:65], v[30:33], v[210:213], v[62:65]
	v_mfma_i32_16x16x64_i8 v[58:61], v[46:49], v[210:213], v[58:61]
	v_mfma_i32_16x16x64_i8 v[38:41], v[30:33], v[218:221], v[38:41]
	v_mfma_i32_16x16x64_i8 v[34:37], v[46:49], v[218:221], v[34:37]
	v_mfma_i32_16x16x64_i8 v[14:17], v[30:33], v[226:229], v[14:17]
	v_mfma_i32_16x16x64_i8 v[10:13], v[46:49], v[226:229], v[10:13]
	v_mfma_i32_16x16x64_i8 v[22:25], v[168:171], v[214:217], v[22:25]
	v_mfma_i32_16x16x64_i8 v[18:21], v[176:179], v[214:217], v[18:21]
	v_mfma_i32_16x16x64_i8 v[6:9], v[168:171], v[222:225], v[6:9]
	v_mfma_i32_16x16x64_i8 v[2:5], v[176:179], v[222:225], v[2:5]
	v_mfma_i32_16x16x64_i8 v[26:29], v[168:171], v[198:201], v[70:73]
	v_mfma_i32_16x16x64_i8 v[30:33], v[176:179], v[198:201], v[66:69]
	v_mfma_i32_16x16x64_i8 v[42:45], v[168:171], v[206:209], v[54:57]
	v_mfma_i32_16x16x64_i8 v[46:49], v[176:179], v[206:209], v[50:53]
	v_mfma_i32_16x16x64_i8 v[22:25], v[172:175], v[218:221], v[22:25]
	v_mfma_i32_16x16x64_i8 v[18:21], v[194:197], v[218:221], v[18:21]
	v_mfma_i32_16x16x64_i8 v[6:9], v[172:175], v[226:229], v[6:9]
	v_mfma_i32_16x16x64_i8 v[2:5], v[194:197], v[226:229], v[2:5]
	v_mfma_i32_16x16x64_i8 v[26:29], v[172:175], v[202:205], v[26:29]
	v_mfma_i32_16x16x64_i8 v[30:33], v[194:197], v[202:205], v[30:33]
	v_mfma_i32_16x16x64_i8 v[42:45], v[172:175], v[210:213], v[42:45]
	v_mfma_i32_16x16x64_i8 v[46:49], v[194:197], v[210:213], v[46:49]
	s_barrier
	s_add_i32 s38, 0, 0x18000
	s_add_i32 s39, 0, 0x1c000
	v_add_u32_e32 v70, s38, v188
	v_add_u32_e32 v154, s39, v188
	ds_read_b128 v[50:53], v70
	ds_read_b128 v[54:57], v70 offset:1024
	ds_read_b128 v[66:69], v70 offset:2048
	ds_read_b128 v[70:73], v70 offset:3072
	ds_read_b128 v[168:171], v154
	ds_read_b128 v[172:175], v154 offset:1024
	ds_read_b128 v[176:179], v154 offset:2048
	ds_read_b128 v[194:197], v154 offset:3072
	s_add_u32 s44, s44, 0x80000
	s_addc_u32 s45, s45, 0
	s_mov_b32 m0, s52
	ds_read_b128 v[198:201], v193 offset:32768
	ds_read_b128 v[202:205], v193 offset:33792
	ds_read_b128 v[206:209], v193 offset:34816
	ds_read_b128 v[210:213], v193 offset:35840
	ds_read_b128 v[214:217], v193 offset:36864
	ds_read_b128 v[218:221], v193 offset:37888
	ds_read_b128 v[222:225], v193 offset:38912
	ds_read_b128 v[226:229], v193 offset:39936
	global_load_lds_dwordx4 v146, s[44:45]
	s_mov_b32 m0, s53
	s_nop 0
	global_load_lds_dwordx4 v150, s[44:45]
	s_waitcnt vmcnt(8)
	s_waitcnt lgkmcnt(0)
	s_barrier
	s_waitcnt lgkmcnt(0)
	v_mfma_i32_16x16x64_i8 v[142:145], v[50:53], v[198:201], v[142:145]
	v_mfma_i32_16x16x64_i8 v[138:141], v[66:69], v[198:201], v[138:141]
	v_mfma_i32_16x16x64_i8 v[126:129], v[50:53], v[206:209], v[126:129]
	v_mfma_i32_16x16x64_i8 v[122:125], v[66:69], v[206:209], v[122:125]
	v_mfma_i32_16x16x64_i8 v[110:113], v[50:53], v[214:217], v[110:113]
	v_mfma_i32_16x16x64_i8 v[106:109], v[66:69], v[214:217], v[106:109]
	v_mfma_i32_16x16x64_i8 v[94:97], v[50:53], v[222:225], v[94:97]
	v_mfma_i32_16x16x64_i8 v[90:93], v[66:69], v[222:225], v[90:93]
	v_mfma_i32_16x16x64_i8 v[142:145], v[54:57], v[202:205], v[142:145]
	v_mfma_i32_16x16x64_i8 v[138:141], v[70:73], v[202:205], v[138:141]
	v_mfma_i32_16x16x64_i8 v[126:129], v[54:57], v[210:213], v[126:129]
	v_mfma_i32_16x16x64_i8 v[122:125], v[70:73], v[210:213], v[122:125]
	v_mfma_i32_16x16x64_i8 v[110:113], v[54:57], v[218:221], v[110:113]
	v_mfma_i32_16x16x64_i8 v[106:109], v[70:73], v[218:221], v[106:109]
	v_mfma_i32_16x16x64_i8 v[94:97], v[54:57], v[226:229], v[94:97]
	v_mfma_i32_16x16x64_i8 v[90:93], v[70:73], v[226:229], v[90:93]
	v_mfma_i32_16x16x64_i8 v[134:137], v[168:171], v[198:201], v[134:137]
	v_mfma_i32_16x16x64_i8 v[130:133], v[176:179], v[198:201], v[130:133]
	v_mfma_i32_16x16x64_i8 v[118:121], v[168:171], v[206:209], v[118:121]
	v_mfma_i32_16x16x64_i8 v[114:117], v[176:179], v[206:209], v[114:117]
	v_mfma_i32_16x16x64_i8 v[102:105], v[168:171], v[214:217], v[102:105]
	v_mfma_i32_16x16x64_i8 v[98:101], v[176:179], v[214:217], v[98:101]
	v_mfma_i32_16x16x64_i8 v[86:89], v[168:171], v[222:225], v[86:89]
	v_mfma_i32_16x16x64_i8 v[82:85], v[176:179], v[222:225], v[82:85]
	v_mfma_i32_16x16x64_i8 v[134:137], v[172:175], v[202:205], v[134:137]
	v_mfma_i32_16x16x64_i8 v[130:133], v[194:197], v[202:205], v[130:133]
	v_mfma_i32_16x16x64_i8 v[118:121], v[172:175], v[210:213], v[118:121]
	v_mfma_i32_16x16x64_i8 v[114:117], v[194:197], v[210:213], v[114:117]
	v_mfma_i32_16x16x64_i8 v[102:105], v[172:175], v[218:221], v[102:105]
	v_mfma_i32_16x16x64_i8 v[98:101], v[194:197], v[218:221], v[98:101]
	v_mfma_i32_16x16x64_i8 v[86:89], v[172:175], v[226:229], v[86:89]
	v_mfma_i32_16x16x64_i8 v[82:85], v[194:197], v[226:229], v[82:85]
	s_barrier
	s_add_i32 s38, s38, s47
	s_mov_b32 m0, s38
	ds_read_b128 v[198:201], v193 offset:49152
	ds_read_b128 v[202:205], v193 offset:50176
	ds_read_b128 v[206:209], v193 offset:51200
	ds_read_b128 v[210:213], v193 offset:52224
	ds_read_b128 v[214:217], v193 offset:53248
	ds_read_b128 v[218:221], v193 offset:54272
	ds_read_b128 v[222:225], v193 offset:55296
	ds_read_b128 v[226:229], v193 offset:56320
	global_load_lds_dwordx4 v148, s[98:99]
	s_add_i32 m0, s38, 0x2000
	s_add_u32 s42, s42, 0x80080
	s_addc_u32 s43, s43, 0
	s_add_i32 s38, s39, s47
	global_load_lds_dwordx4 v152, s[98:99]
	s_mov_b32 m0, s38
	s_nop 0
	global_load_lds_dwordx4 v148, s[42:43]
	s_add_i32 m0, s38, 0x2000
	s_nop 0
	global_load_lds_dwordx4 v152, s[42:43]
	s_mov_b32 m0, s58
	s_nop 0
	global_load_lds_dwordx4 v146, s[100:101]
	s_mov_b32 m0, s59
	s_nop 0
	global_load_lds_dwordx4 v150, s[100:101]
	s_waitcnt vmcnt(8)
	s_waitcnt lgkmcnt(0)
	s_barrier
	s_waitcnt lgkmcnt(0)
	v_mfma_i32_16x16x64_i8 v[78:81], v[50:53], v[198:201], v[78:81]
	v_mfma_i32_16x16x64_i8 v[74:77], v[66:69], v[198:201], v[74:77]
	v_mfma_i32_16x16x64_i8 v[62:65], v[50:53], v[206:209], v[62:65]
	v_mfma_i32_16x16x64_i8 v[58:61], v[66:69], v[206:209], v[58:61]
	v_mfma_i32_16x16x64_i8 v[38:41], v[50:53], v[214:217], v[38:41]
	v_mfma_i32_16x16x64_i8 v[34:37], v[66:69], v[214:217], v[34:37]
	v_mfma_i32_16x16x64_i8 v[14:17], v[50:53], v[222:225], v[14:17]
	v_mfma_i32_16x16x64_i8 v[10:13], v[66:69], v[222:225], v[10:13]
	v_mfma_i32_16x16x64_i8 v[78:81], v[54:57], v[202:205], v[78:81]
	v_mfma_i32_16x16x64_i8 v[74:77], v[70:73], v[202:205], v[74:77]
	v_mfma_i32_16x16x64_i8 v[62:65], v[54:57], v[210:213], v[62:65]
	v_mfma_i32_16x16x64_i8 v[58:61], v[70:73], v[210:213], v[58:61]
	v_mfma_i32_16x16x64_i8 v[38:41], v[54:57], v[218:221], v[38:41]
	v_mfma_i32_16x16x64_i8 v[34:37], v[70:73], v[218:221], v[34:37]
	v_mfma_i32_16x16x64_i8 v[14:17], v[54:57], v[226:229], v[14:17]
	v_mfma_i32_16x16x64_i8 v[10:13], v[70:73], v[226:229], v[10:13]
	v_mfma_i32_16x16x64_i8 v[26:29], v[168:171], v[198:201], v[26:29]
	v_mfma_i32_16x16x64_i8 v[70:73], v[172:175], v[202:205], v[26:29]
	v_mfma_i32_16x16x64_i8 v[26:29], v[176:179], v[198:201], v[30:33]
	v_mfma_i32_16x16x64_i8 v[66:69], v[194:197], v[202:205], v[26:29]
	v_mfma_i32_16x16x64_i8 v[26:29], v[168:171], v[206:209], v[42:45]
	v_mfma_i32_16x16x64_i8 v[54:57], v[172:175], v[210:213], v[26:29]
	v_mfma_i32_16x16x64_i8 v[26:29], v[176:179], v[206:209], v[46:49]
	v_mfma_i32_16x16x64_i8 v[22:25], v[168:171], v[214:217], v[22:25]
	v_mfma_i32_16x16x64_i8 v[18:21], v[176:179], v[214:217], v[18:21]
	v_mfma_i32_16x16x64_i8 v[6:9], v[168:171], v[222:225], v[6:9]
	v_mfma_i32_16x16x64_i8 v[2:5], v[176:179], v[222:225], v[2:5]
	v_mfma_i32_16x16x64_i8 v[50:53], v[194:197], v[210:213], v[26:29]
	v_mfma_i32_16x16x64_i8 v[22:25], v[172:175], v[218:221], v[22:25]
	v_mfma_i32_16x16x64_i8 v[18:21], v[194:197], v[218:221], v[18:21]
	v_mfma_i32_16x16x64_i8 v[6:9], v[172:175], v[226:229], v[6:9]
	v_mfma_i32_16x16x64_i8 v[2:5], v[194:197], v[226:229], v[2:5]
	s_barrier
	s_add_i32 s74, s74, 2
	s_add_u32 s34, s34, 0x100
	s_addc_u32 s35, s35, 0
	s_add_u32 s67, s67, 0x100
	s_addc_u32 s73, s73, 0
	s_cmp_gt_u32 s74, 29
	s_cbranch_scc0 .LBB0_547
	s_and_b64 vcc, exec, s[14:15]
	s_cbranch_vccz .LBB0_550
	s_barrier

.Lprio_P2c:
.LBB0_673:
	ds_read_b128 v[122:125], v167
	ds_read_b128 v[126:129], v167 offset:1024
	ds_read_b128 v[130:133], v167 offset:2048
	ds_read_b128 v[134:137], v167 offset:3072
	ds_read_b128 v[174:177], v171
	ds_read_b128 v[178:181], v171 offset:1024
	ds_read_b128 v[182:185], v171 offset:2048
	ds_read_b128 v[186:189], v171 offset:3072
	s_add_u32 s38, s44, 0xfff80080
	s_addc_u32 s39, s45, -1
	s_cmp_eq_u32 s77, 28
	s_cselect_b32 s47, s25, s39
	s_cselect_b32 s46, s73, s38
	s_cselect_b32 s43, s15, s76
	s_cselect_b32 s42, s74, s75
	s_add_i32 m0, s35, 0xc000
	ds_read_b128 v[190:193], v172
	ds_read_b128 v[194:197], v172 offset:1024
	ds_read_b128 v[198:201], v172 offset:2048
	ds_read_b128 v[202:205], v172 offset:3072
	ds_read_b128 v[206:209], v172 offset:4096
	ds_read_b128 v[210:213], v172 offset:5120
	ds_read_b128 v[214:217], v172 offset:6144
	ds_read_b128 v[218:221], v172 offset:7168
	global_load_lds_dwordx4 v156, s[44:45]
	s_add_i32 m0, s35, 0xe000
	s_nop 0
	global_load_lds_dwordx4 v158, s[44:45]
	s_waitcnt vmcnt(8)
	s_waitcnt lgkmcnt(0)
	s_barrier
	s_waitcnt lgkmcnt(0)
	v_mfma_i32_16x16x64_i8 v[142:145], v[122:125], v[190:193], v[142:145]
	v_mfma_i32_16x16x64_i8 v[138:141], v[130:133], v[190:193], v[138:141]
	v_mfma_i32_16x16x64_i8 v[110:113], v[122:125], v[198:201], v[110:113]
	v_mfma_i32_16x16x64_i8 v[106:109], v[130:133], v[198:201], v[106:109]
	v_mfma_i32_16x16x64_i8 v[94:97], v[122:125], v[206:209], v[94:97]
	v_mfma_i32_16x16x64_i8 v[90:93], v[130:133], v[206:209], v[90:93]
	v_mfma_i32_16x16x64_i8 v[78:81], v[122:125], v[214:217], v[78:81]
	v_mfma_i32_16x16x64_i8 v[74:77], v[130:133], v[214:217], v[74:77]
	v_mfma_i32_16x16x64_i8 v[142:145], v[126:129], v[194:197], v[142:145]
	v_mfma_i32_16x16x64_i8 v[138:141], v[134:137], v[194:197], v[138:141]
	v_mfma_i32_16x16x64_i8 v[110:113], v[126:129], v[202:205], v[110:113]
	v_mfma_i32_16x16x64_i8 v[106:109], v[134:137], v[202:205], v[106:109]
	v_mfma_i32_16x16x64_i8 v[94:97], v[126:129], v[210:213], v[94:97]
	v_mfma_i32_16x16x64_i8 v[90:93], v[134:137], v[210:213], v[90:93]
	v_mfma_i32_16x16x64_i8 v[78:81], v[126:129], v[218:221], v[78:81]
	v_mfma_i32_16x16x64_i8 v[74:77], v[134:137], v[218:221], v[74:77]
	v_mfma_i32_16x16x64_i8 v[118:121], v[174:177], v[190:193], v[118:121]
	v_mfma_i32_16x16x64_i8 v[114:117], v[182:185], v[190:193], v[114:117]
	v_mfma_i32_16x16x64_i8 v[102:105], v[174:177], v[198:201], v[102:105]
	v_mfma_i32_16x16x64_i8 v[98:101], v[182:185], v[198:201], v[98:101]
	v_mfma_i32_16x16x64_i8 v[86:89], v[174:177], v[206:209], v[86:89]
	v_mfma_i32_16x16x64_i8 v[82:85], v[182:185], v[206:209], v[82:85]
	v_mfma_i32_16x16x64_i8 v[70:73], v[174:177], v[214:217], v[70:73]
	v_mfma_i32_16x16x64_i8 v[66:69], v[182:185], v[214:217], v[66:69]
	v_mfma_i32_16x16x64_i8 v[118:121], v[178:181], v[194:197], v[118:121]
	v_mfma_i32_16x16x64_i8 v[114:117], v[186:189], v[194:197], v[114:117]
	v_mfma_i32_16x16x64_i8 v[102:105], v[178:181], v[202:205], v[102:105]
	v_mfma_i32_16x16x64_i8 v[98:101], v[186:189], v[202:205], v[98:101]
	v_mfma_i32_16x16x64_i8 v[86:89], v[178:181], v[210:213], v[86:89]
	v_mfma_i32_16x16x64_i8 v[82:85], v[186:189], v[210:213], v[82:85]
	v_mfma_i32_16x16x64_i8 v[70:73], v[178:181], v[218:221], v[70:73]
	v_mfma_i32_16x16x64_i8 v[66:69], v[186:189], v[218:221], v[66:69]
	s_barrier
	s_add_u32 s98, s42, s6
	s_addc_u32 s99, s43, s7
	s_add_u32 s100, s46, s6
	s_addc_u32 s101, s47, s7
	s_add_i32 s38, s66, s52
	s_mov_b32 m0, s38
	ds_read_b128 v[190:193], v172 offset:16384
	ds_read_b128 v[194:197], v172 offset:17408
	ds_read_b128 v[198:201], v172 offset:18432
	ds_read_b128 v[202:205], v172 offset:19456
	ds_read_b128 v[206:209], v172 offset:20480
	ds_read_b128 v[210:213], v172 offset:21504
	ds_read_b128 v[214:217], v172 offset:22528
	ds_read_b128 v[218:221], v172 offset:23552
	global_load_lds_dwordx4 v148, s[42:43]
	s_add_i32 m0, s38, 0x2000
	s_add_u32 s78, s42, 0x80000
	s_addc_u32 s79, s43, 0
	s_add_i32 s38, s67, s52
	global_load_lds_dwordx4 v152, s[42:43]
	s_mov_b32 m0, s38
	s_nop 0
	global_load_lds_dwordx4 v148, s[78:79]
	s_add_i32 m0, s38, 0x2000
	s_nop 0
	global_load_lds_dwordx4 v152, s[78:79]
	s_mov_b32 m0, s35
	s_nop 0
	global_load_lds_dwordx4 v146, s[46:47]
	s_mov_b32 m0, s53
	s_nop 0
	global_load_lds_dwordx4 v150, s[46:47]
	s_waitcnt vmcnt(8)
	s_waitcnt lgkmcnt(0)
	s_barrier
	s_waitcnt lgkmcnt(0)
	v_mfma_i32_16x16x64_i8 v[62:65], v[122:125], v[190:193], v[62:65]
	v_mfma_i32_16x16x64_i8 v[58:61], v[130:133], v[190:193], v[58:61]
	v_mfma_i32_16x16x64_i8 v[46:49], v[122:125], v[198:201], v[46:49]
	v_mfma_i32_16x16x64_i8 v[42:45], v[130:133], v[198:201], v[42:45]
	v_mfma_i32_16x16x64_i8 v[30:33], v[122:125], v[206:209], v[30:33]
	v_mfma_i32_16x16x64_i8 v[26:29], v[130:133], v[206:209], v[26:29]
	v_mfma_i32_16x16x64_i8 v[14:17], v[122:125], v[214:217], v[14:17]
	v_mfma_i32_16x16x64_i8 v[10:13], v[130:133], v[214:217], v[10:13]
	v_mfma_i32_16x16x64_i8 v[62:65], v[126:129], v[194:197], v[62:65]
	v_mfma_i32_16x16x64_i8 v[58:61], v[134:137], v[194:197], v[58:61]
	v_mfma_i32_16x16x64_i8 v[46:49], v[126:129], v[202:205], v[46:49]
	v_mfma_i32_16x16x64_i8 v[42:45], v[134:137], v[202:205], v[42:45]
	v_mfma_i32_16x16x64_i8 v[30:33], v[126:129], v[210:213], v[30:33]
	v_mfma_i32_16x16x64_i8 v[26:29], v[134:137], v[210:213], v[26:29]
	v_mfma_i32_16x16x64_i8 v[14:17], v[126:129], v[218:221], v[14:17]
	v_mfma_i32_16x16x64_i8 v[10:13], v[134:137], v[218:221], v[10:13]
	v_mfma_i32_16x16x64_i8 v[54:57], v[174:177], v[190:193], v[54:57]
	v_mfma_i32_16x16x64_i8 v[50:53], v[182:185], v[190:193], v[50:53]
	v_mfma_i32_16x16x64_i8 v[38:41], v[174:177], v[198:201], v[38:41]
	v_mfma_i32_16x16x64_i8 v[34:37], v[182:185], v[198:201], v[34:37]
	v_mfma_i32_16x16x64_i8 v[22:25], v[174:177], v[206:209], v[22:25]
	v_mfma_i32_16x16x64_i8 v[18:21], v[182:185], v[206:209], v[18:21]
	v_mfma_i32_16x16x64_i8 v[6:9], v[174:177], v[214:217], v[6:9]
	v_mfma_i32_16x16x64_i8 v[2:5], v[182:185], v[214:217], v[2:5]
	v_mfma_i32_16x16x64_i8 v[54:57], v[178:181], v[194:197], v[54:57]
	v_mfma_i32_16x16x64_i8 v[50:53], v[186:189], v[194:197], v[50:53]
	v_mfma_i32_16x16x64_i8 v[38:41], v[178:181], v[202:205], v[38:41]
	v_mfma_i32_16x16x64_i8 v[34:37], v[186:189], v[202:205], v[34:37]
	v_mfma_i32_16x16x64_i8 v[22:25], v[178:181], v[210:213], v[22:25]
	v_mfma_i32_16x16x64_i8 v[18:21], v[186:189], v[210:213], v[18:21]
	v_mfma_i32_16x16x64_i8 v[6:9], v[178:181], v[218:221], v[6:9]
	v_mfma_i32_16x16x64_i8 v[2:5], v[186:189], v[218:221], v[2:5]
	s_barrier
	s_add_i32 s38, 0, 0x18000
	s_add_i32 s39, 0, 0x1c000
	v_add_u32_e32 v134, s38, v169
	v_add_u32_e32 v154, s39, v169
	ds_read_b128 v[122:125], v134
	ds_read_b128 v[126:129], v134 offset:1024
	ds_read_b128 v[130:133], v134 offset:2048
	ds_read_b128 v[134:137], v134 offset:3072
	ds_read_b128 v[174:177], v154
	ds_read_b128 v[178:181], v154 offset:1024
	ds_read_b128 v[182:185], v154 offset:2048
	ds_read_b128 v[186:189], v154 offset:3072
	s_add_u32 s46, s46, 0x80000
	s_addc_u32 s47, s47, 0
	s_mov_b32 m0, s58
	ds_read_b128 v[190:193], v172 offset:32768
	ds_read_b128 v[194:197], v172 offset:33792
	ds_read_b128 v[198:201], v172 offset:34816
	ds_read_b128 v[202:205], v172 offset:35840
	ds_read_b128 v[206:209], v172 offset:36864
	ds_read_b128 v[210:213], v172 offset:37888
	ds_read_b128 v[214:217], v172 offset:38912
	ds_read_b128 v[218:221], v172 offset:39936
	global_load_lds_dwordx4 v146, s[46:47]
	s_mov_b32 m0, s59
	s_nop 0
	global_load_lds_dwordx4 v150, s[46:47]
	s_waitcnt vmcnt(8)
	s_waitcnt lgkmcnt(0)
	s_barrier
	s_waitcnt lgkmcnt(0)
	v_mfma_i32_16x16x64_i8 v[142:145], v[122:125], v[190:193], v[142:145]
	v_mfma_i32_16x16x64_i8 v[138:141], v[130:133], v[190:193], v[138:141]
	v_mfma_i32_16x16x64_i8 v[110:113], v[122:125], v[198:201], v[110:113]
	v_mfma_i32_16x16x64_i8 v[106:109], v[130:133], v[198:201], v[106:109]
	v_mfma_i32_16x16x64_i8 v[94:97], v[122:125], v[206:209], v[94:97]
	v_mfma_i32_16x16x64_i8 v[90:93], v[130:133], v[206:209], v[90:93]
	v_mfma_i32_16x16x64_i8 v[78:81], v[122:125], v[214:217], v[78:81]
	v_mfma_i32_16x16x64_i8 v[74:77], v[130:133], v[214:217], v[74:77]
	v_mfma_i32_16x16x64_i8 v[142:145], v[126:129], v[194:197], v[142:145]
	v_mfma_i32_16x16x64_i8 v[138:141], v[134:137], v[194:197], v[138:141]
	v_mfma_i32_16x16x64_i8 v[110:113], v[126:129], v[202:205], v[110:113]
	v_mfma_i32_16x16x64_i8 v[106:109], v[134:137], v[202:205], v[106:109]
	v_mfma_i32_16x16x64_i8 v[94:97], v[126:129], v[210:213], v[94:97]
	v_mfma_i32_16x16x64_i8 v[90:93], v[134:137], v[210:213], v[90:93]
	v_mfma_i32_16x16x64_i8 v[78:81], v[126:129], v[218:221], v[78:81]
	v_mfma_i32_16x16x64_i8 v[74:77], v[134:137], v[218:221], v[74:77]
	v_mfma_i32_16x16x64_i8 v[118:121], v[174:177], v[190:193], v[118:121]
	v_mfma_i32_16x16x64_i8 v[114:117], v[182:185], v[190:193], v[114:117]
	v_mfma_i32_16x16x64_i8 v[102:105], v[174:177], v[198:201], v[102:105]
	v_mfma_i32_16x16x64_i8 v[98:101], v[182:185], v[198:201], v[98:101]
	v_mfma_i32_16x16x64_i8 v[86:89], v[174:177], v[206:209], v[86:89]
	v_mfma_i32_16x16x64_i8 v[82:85], v[182:185], v[206:209], v[82:85]
	v_mfma_i32_16x16x64_i8 v[70:73], v[174:177], v[214:217], v[70:73]
	v_mfma_i32_16x16x64_i8 v[66:69], v[182:185], v[214:217], v[66:69]
	v_mfma_i32_16x16x64_i8 v[118:121], v[178:181], v[194:197], v[118:121]
	v_mfma_i32_16x16x64_i8 v[114:117], v[186:189], v[194:197], v[114:117]
	v_mfma_i32_16x16x64_i8 v[102:105], v[178:181], v[202:205], v[102:105]
	v_mfma_i32_16x16x64_i8 v[98:101], v[186:189], v[202:205], v[98:101]
	v_mfma_i32_16x16x64_i8 v[86:89], v[178:181], v[210:213], v[86:89]
	v_mfma_i32_16x16x64_i8 v[82:85], v[186:189], v[210:213], v[82:85]
	v_mfma_i32_16x16x64_i8 v[70:73], v[178:181], v[218:221], v[70:73]
	v_mfma_i32_16x16x64_i8 v[66:69], v[186:189], v[218:221], v[66:69]
	s_barrier
	s_add_i32 s38, s38, s52
	s_mov_b32 m0, s38
	ds_read_b128 v[190:193], v172 offset:49152
	ds_read_b128 v[194:197], v172 offset:50176
	ds_read_b128 v[198:201], v172 offset:51200
	ds_read_b128 v[202:205], v172 offset:52224
	ds_read_b128 v[206:209], v172 offset:53248
	ds_read_b128 v[210:213], v172 offset:54272
	ds_read_b128 v[214:217], v172 offset:55296
	ds_read_b128 v[218:221], v172 offset:56320
	global_load_lds_dwordx4 v148, s[98:99]
	s_add_i32 m0, s38, 0x2000
	s_add_u32 s42, s42, 0x80080
	s_addc_u32 s43, s43, 0
	s_add_i32 s38, s39, s52
	global_load_lds_dwordx4 v152, s[98:99]
	s_mov_b32 m0, s38
	s_nop 0
	global_load_lds_dwordx4 v148, s[42:43]
	s_add_i32 m0, s38, 0x2000
	s_nop 0
	global_load_lds_dwordx4 v152, s[42:43]
	s_mov_b32 m0, s61
	s_nop 0
	global_load_lds_dwordx4 v146, s[100:101]
	s_mov_b32 m0, s62
	s_nop 0
	global_load_lds_dwordx4 v150, s[100:101]
	s_waitcnt vmcnt(8)
	s_waitcnt lgkmcnt(0)
	s_barrier
	s_waitcnt lgkmcnt(0)
	v_mfma_i32_16x16x64_i8 v[62:65], v[122:125], v[190:193], v[62:65]
	v_mfma_i32_16x16x64_i8 v[58:61], v[130:133], v[190:193], v[58:61]
	v_mfma_i32_16x16x64_i8 v[46:49], v[122:125], v[198:201], v[46:49]
	v_mfma_i32_16x16x64_i8 v[42:45], v[130:133], v[198:201], v[42:45]
	v_mfma_i32_16x16x64_i8 v[30:33], v[122:125], v[206:209], v[30:33]
	v_mfma_i32_16x16x64_i8 v[26:29], v[130:133], v[206:209], v[26:29]
	v_mfma_i32_16x16x64_i8 v[14:17], v[122:125], v[214:217], v[14:17]
	v_mfma_i32_16x16x64_i8 v[10:13], v[130:133], v[214:217], v[10:13]
	v_mfma_i32_16x16x64_i8 v[62:65], v[126:129], v[194:197], v[62:65]
	v_mfma_i32_16x16x64_i8 v[58:61], v[134:137], v[194:197], v[58:61]
	v_mfma_i32_16x16x64_i8 v[46:49], v[126:129], v[202:205], v[46:49]
	v_mfma_i32_16x16x64_i8 v[42:45], v[134:137], v[202:205], v[42:45]
	v_mfma_i32_16x16x64_i8 v[30:33], v[126:129], v[210:213], v[30:33]
	v_mfma_i32_16x16x64_i8 v[26:29], v[134:137], v[210:213], v[26:29]
	v_mfma_i32_16x16x64_i8 v[14:17], v[126:129], v[218:221], v[14:17]
	v_mfma_i32_16x16x64_i8 v[10:13], v[134:137], v[218:221], v[10:13]
	v_mfma_i32_16x16x64_i8 v[54:57], v[174:177], v[190:193], v[54:57]
	v_mfma_i32_16x16x64_i8 v[50:53], v[182:185], v[190:193], v[50:53]
	v_mfma_i32_16x16x64_i8 v[38:41], v[174:177], v[198:201], v[38:41]
	v_mfma_i32_16x16x64_i8 v[34:37], v[182:185], v[198:201], v[34:37]
	v_mfma_i32_16x16x64_i8 v[22:25], v[174:177], v[206:209], v[22:25]
	v_mfma_i32_16x16x64_i8 v[18:21], v[182:185], v[206:209], v[18:21]
	v_mfma_i32_16x16x64_i8 v[6:9], v[174:177], v[214:217], v[6:9]
	v_mfma_i32_16x16x64_i8 v[2:5], v[182:185], v[214:217], v[2:5]
	v_mfma_i32_16x16x64_i8 v[54:57], v[178:181], v[194:197], v[54:57]
	v_mfma_i32_16x16x64_i8 v[50:53], v[186:189], v[194:197], v[50:53]
	v_mfma_i32_16x16x64_i8 v[38:41], v[178:181], v[202:205], v[38:41]
	v_mfma_i32_16x16x64_i8 v[34:37], v[186:189], v[202:205], v[34:37]
	v_mfma_i32_16x16x64_i8 v[22:25], v[178:181], v[210:213], v[22:25]
	v_mfma_i32_16x16x64_i8 v[18:21], v[186:189], v[210:213], v[18:21]
	v_mfma_i32_16x16x64_i8 v[6:9], v[178:181], v[218:221], v[6:9]
	v_mfma_i32_16x16x64_i8 v[2:5], v[186:189], v[218:221], v[2:5]
	s_barrier
	s_add_i32 s77, s77, 2
	s_add_u32 s44, s44, 0x100
	s_addc_u32 s45, s45, 0
	s_add_u32 s75, s75, 0x100
	s_addc_u32 s76, s76, 0
	s_cmp_gt_u32 s77, 29
	s_cbranch_scc0 .LBB0_673
	s_and_b64 vcc, exec, s[8:9]
	s_cbranch_vccz .LBB0_676
	s_barrier

.LBB0_734:
	s_setprio 0
	s_cmp_lt_i32 s70, 4
	s_cselect_b64 s[0:1], -1, 0
	s_add_u32 s4, s68, 0x500000
	s_addc_u32 s5, s69, 0
	s_add_u32 s60, s68, 0x300000
	v_writelane_b32 v255, s4, 5
	s_addc_u32 s61, s69, 0
	s_nop 0
	v_writelane_b32 v255, s5, 6
	s_add_u32 s4, s68, 0x400000
	s_addc_u32 s5, s69, 0
	v_writelane_b32 v255, s4, 7
	s_nop 1
	v_writelane_b32 v255, s5, 8
	s_and_b64 s[4:5], s[0:1], s[2:3]
	s_xor_b64 s[0:1], s[4:5], -1
	s_cmpk_gt_i32 s90, 0xff
	s_cselect_b64 s[2:3], -1, 0
	s_or_b64 s[0:1], s[2:3], s[0:1]
	s_and_b64 vcc, exec, s[0:1]
	s_cbranch_vccnz .LBB0_839
	v_and_b32_e32 v89, 15, v0
	s_lshl_b32 s0, s92, 9
	v_readlane_b32 s2, v254, 39
	v_readlane_b32 s6, v255, 5
	s_mov_b32 s1, 0
	s_cmpk_lt_u32 s2, 0x300
	v_lshlrev_b32_e32 v86, 2, v89
	v_mov_b32_e32 v87, 0
	v_readlane_b32 s7, v255, 6
	s_cselect_b64 s[2:3], -1, 0
	v_lshlrev_b32_e32 v4, 4, v166
	v_lshl_add_u64 v[50:51], s[6:7], 0, v[86:87]
	s_lshl_b64 s[6:7], s[0:1], 1
	s_add_u32 s6, s68, s6
	v_and_b32_e32 v86, 48, v0
	s_addc_u32 s7, s69, s7
	s_lshl_b32 s0, s92, 10
	v_lshrrev_b32_e32 v60, 4, v166
	v_add_u32_e32 v5, 0, v4
	s_mul_i32 s15, s92, 0x3000
	s_lshl_b32 s33, s90, 6
	v_lshl_or_b32 v2, v89, 13, v86
	v_mov_b32_e32 v3, v87
	s_add_i32 s0, s0, 0
	v_lshlrev_b32_e32 v118, 2, v60
	v_lshl_add_u64 v[52:53], s[6:7], 0, v[86:87]
	v_or_b32_e32 v54, s33, v89
	s_lshl_b32 s34, s91, 6
	v_lshl_add_u64 v[56:57], s[6:7], 0, v[2:3]
	s_lshl_b32 s35, s92, 4
	v_add_u32_e32 v61, s0, v4
	s_mov_b32 s8, 0x1da00000
	s_mov_b32 s9, 0x1da20000
	s_mov_b32 s10, 0x1da40000
	s_mov_b32 s11, 0x1da60000
	s_mov_b32 s12, 0x280000
	s_mov_b32 s13, 0x2a0000
	s_mov_b32 s14, 0x2c0000
	v_add_u32_e32 v62, s15, v5
	s_movk_i32 s15, 0xc0
	s_mov_b32 s24, s90
	s_branch .LBB0_737

.Lprio_P6:
.LBB0_1489:
	ds_read_b128 v[122:125], v169
	ds_read_b128 v[126:129], v169 offset:1024
	ds_read_b128 v[130:133], v169 offset:2048
	ds_read_b128 v[134:137], v169 offset:3072
	ds_read_b128 v[172:175], v170
	ds_read_b128 v[176:179], v170 offset:1024
	ds_read_b128 v[180:183], v170 offset:2048
	ds_read_b128 v[184:187], v170 offset:3072
	s_add_u32 s26, s24, 0xfff80080
	s_addc_u32 s27, s25, -1
	s_cmp_eq_u32 s53, 28
	s_cselect_b32 s29, s17, s27
	s_cselect_b32 s28, s49, s26
	s_cselect_b32 s27, s15, s52
	s_cselect_b32 s26, s50, s51
	s_add_i32 m0, s23, 0xc000
	ds_read_b128 v[188:191], v171
	ds_read_b128 v[192:195], v171 offset:1024
	ds_read_b128 v[196:199], v171 offset:2048
	ds_read_b128 v[200:203], v171 offset:3072
	ds_read_b128 v[204:207], v171 offset:4096
	ds_read_b128 v[208:211], v171 offset:5120
	ds_read_b128 v[212:215], v171 offset:6144
	ds_read_b128 v[216:219], v171 offset:7168
	global_load_lds_dwordx4 v156, s[24:25]
	s_add_i32 m0, s23, 0xe000
	s_nop 0
	global_load_lds_dwordx4 v158, s[24:25]
	s_waitcnt vmcnt(8)
	s_waitcnt lgkmcnt(0)
	s_barrier
	s_waitcnt lgkmcnt(0)
	v_mfma_i32_16x16x64_i8 v[142:145], v[122:125], v[188:191], v[142:145]
	v_mfma_i32_16x16x64_i8 v[138:141], v[130:133], v[188:191], v[138:141]
	v_mfma_i32_16x16x64_i8 v[110:113], v[122:125], v[196:199], v[110:113]
	v_mfma_i32_16x16x64_i8 v[106:109], v[130:133], v[196:199], v[106:109]
	v_mfma_i32_16x16x64_i8 v[94:97], v[122:125], v[204:207], v[94:97]
	v_mfma_i32_16x16x64_i8 v[90:93], v[130:133], v[204:207], v[90:93]
	v_mfma_i32_16x16x64_i8 v[78:81], v[122:125], v[212:215], v[78:81]
	v_mfma_i32_16x16x64_i8 v[74:77], v[130:133], v[212:215], v[74:77]
	v_mfma_i32_16x16x64_i8 v[142:145], v[126:129], v[192:195], v[142:145]
	v_mfma_i32_16x16x64_i8 v[138:141], v[134:137], v[192:195], v[138:141]
	v_mfma_i32_16x16x64_i8 v[110:113], v[126:129], v[200:203], v[110:113]
	v_mfma_i32_16x16x64_i8 v[106:109], v[134:137], v[200:203], v[106:109]
	v_mfma_i32_16x16x64_i8 v[94:97], v[126:129], v[208:211], v[94:97]
	v_mfma_i32_16x16x64_i8 v[90:93], v[134:137], v[208:211], v[90:93]
	v_mfma_i32_16x16x64_i8 v[78:81], v[126:129], v[216:219], v[78:81]
	v_mfma_i32_16x16x64_i8 v[74:77], v[134:137], v[216:219], v[74:77]
	v_mfma_i32_16x16x64_i8 v[118:121], v[172:175], v[188:191], v[118:121]
	v_mfma_i32_16x16x64_i8 v[114:117], v[180:183], v[188:191], v[114:117]
	v_mfma_i32_16x16x64_i8 v[102:105], v[172:175], v[196:199], v[102:105]
	v_mfma_i32_16x16x64_i8 v[98:101], v[180:183], v[196:199], v[98:101]
	v_mfma_i32_16x16x64_i8 v[86:89], v[172:175], v[204:207], v[86:89]
	v_mfma_i32_16x16x64_i8 v[82:85], v[180:183], v[204:207], v[82:85]
	v_mfma_i32_16x16x64_i8 v[70:73], v[172:175], v[212:215], v[70:73]
	v_mfma_i32_16x16x64_i8 v[66:69], v[180:183], v[212:215], v[66:69]
	v_mfma_i32_16x16x64_i8 v[118:121], v[176:179], v[192:195], v[118:121]
	v_mfma_i32_16x16x64_i8 v[114:117], v[184:187], v[192:195], v[114:117]
	v_mfma_i32_16x16x64_i8 v[102:105], v[176:179], v[200:203], v[102:105]
	v_mfma_i32_16x16x64_i8 v[98:101], v[184:187], v[200:203], v[98:101]
	v_mfma_i32_16x16x64_i8 v[86:89], v[176:179], v[208:211], v[86:89]
	v_mfma_i32_16x16x64_i8 v[82:85], v[184:187], v[208:211], v[82:85]
	v_mfma_i32_16x16x64_i8 v[70:73], v[176:179], v[216:219], v[70:73]
	v_mfma_i32_16x16x64_i8 v[66:69], v[184:187], v[216:219], v[66:69]
	s_barrier
	s_add_u32 s98, s26, s10
	s_addc_u32 s99, s27, s11
	s_add_u32 s100, s28, s10
	s_addc_u32 s101, s29, s11
	s_add_i32 s38, s46, s34
	s_mov_b32 m0, s38
	ds_read_b128 v[188:191], v171 offset:16384
	ds_read_b128 v[192:195], v171 offset:17408
	ds_read_b128 v[196:199], v171 offset:18432
	ds_read_b128 v[200:203], v171 offset:19456
	ds_read_b128 v[204:207], v171 offset:20480
	ds_read_b128 v[208:211], v171 offset:21504
	ds_read_b128 v[212:215], v171 offset:22528
	ds_read_b128 v[216:219], v171 offset:23552
	global_load_lds_dwordx4 v148, s[26:27]
	s_add_i32 m0, s38, 0x2000
	s_add_u32 s38, s26, 0x80000
	s_addc_u32 s39, s27, 0
	s_add_i32 s54, s47, s34
	global_load_lds_dwordx4 v152, s[26:27]
	s_mov_b32 m0, s54
	s_nop 0
	global_load_lds_dwordx4 v148, s[38:39]
	s_add_i32 m0, s54, 0x2000
	s_nop 0
	global_load_lds_dwordx4 v152, s[38:39]
	s_mov_b32 m0, s23
	s_nop 0
	global_load_lds_dwordx4 v146, s[28:29]
	s_mov_b32 m0, s35
	s_nop 0
	global_load_lds_dwordx4 v150, s[28:29]
	s_waitcnt vmcnt(8)
	s_waitcnt lgkmcnt(0)
	s_barrier
	s_waitcnt lgkmcnt(0)
	v_mfma_i32_16x16x64_i8 v[62:65], v[122:125], v[188:191], v[62:65]
	v_mfma_i32_16x16x64_i8 v[58:61], v[130:133], v[188:191], v[58:61]
	v_mfma_i32_16x16x64_i8 v[46:49], v[122:125], v[196:199], v[46:49]
	v_mfma_i32_16x16x64_i8 v[42:45], v[130:133], v[196:199], v[42:45]
	v_mfma_i32_16x16x64_i8 v[30:33], v[122:125], v[204:207], v[30:33]
	v_mfma_i32_16x16x64_i8 v[26:29], v[130:133], v[204:207], v[26:29]
	v_mfma_i32_16x16x64_i8 v[14:17], v[122:125], v[212:215], v[14:17]
	v_mfma_i32_16x16x64_i8 v[10:13], v[130:133], v[212:215], v[10:13]
	v_mfma_i32_16x16x64_i8 v[62:65], v[126:129], v[192:195], v[62:65]
	v_mfma_i32_16x16x64_i8 v[58:61], v[134:137], v[192:195], v[58:61]
	v_mfma_i32_16x16x64_i8 v[46:49], v[126:129], v[200:203], v[46:49]
	v_mfma_i32_16x16x64_i8 v[42:45], v[134:137], v[200:203], v[42:45]
	v_mfma_i32_16x16x64_i8 v[30:33], v[126:129], v[208:211], v[30:33]
	v_mfma_i32_16x16x64_i8 v[26:29], v[134:137], v[208:211], v[26:29]
	v_mfma_i32_16x16x64_i8 v[14:17], v[126:129], v[216:219], v[14:17]
	v_mfma_i32_16x16x64_i8 v[10:13], v[134:137], v[216:219], v[10:13]
	v_mfma_i32_16x16x64_i8 v[54:57], v[172:175], v[188:191], v[54:57]
	v_mfma_i32_16x16x64_i8 v[50:53], v[180:183], v[188:191], v[50:53]
	v_mfma_i32_16x16x64_i8 v[38:41], v[172:175], v[196:199], v[38:41]
	v_mfma_i32_16x16x64_i8 v[34:37], v[180:183], v[196:199], v[34:37]
	v_mfma_i32_16x16x64_i8 v[22:25], v[172:175], v[204:207], v[22:25]
	v_mfma_i32_16x16x64_i8 v[18:21], v[180:183], v[204:207], v[18:21]
	v_mfma_i32_16x16x64_i8 v[6:9], v[172:175], v[212:215], v[6:9]
	v_mfma_i32_16x16x64_i8 v[2:5], v[180:183], v[212:215], v[2:5]
	v_mfma_i32_16x16x64_i8 v[54:57], v[176:179], v[192:195], v[54:57]
	v_mfma_i32_16x16x64_i8 v[50:53], v[184:187], v[192:195], v[50:53]
	v_mfma_i32_16x16x64_i8 v[38:41], v[176:179], v[200:203], v[38:41]
	v_mfma_i32_16x16x64_i8 v[34:37], v[184:187], v[200:203], v[34:37]
	v_mfma_i32_16x16x64_i8 v[22:25], v[176:179], v[208:211], v[22:25]
	v_mfma_i32_16x16x64_i8 v[18:21], v[184:187], v[208:211], v[18:21]
	v_mfma_i32_16x16x64_i8 v[6:9], v[176:179], v[216:219], v[6:9]
	v_mfma_i32_16x16x64_i8 v[2:5], v[184:187], v[216:219], v[2:5]
	s_barrier
	s_add_i32 s38, 0, 0x18000
	s_add_i32 s39, 0, 0x1c000
	v_add_u32_e32 v134, s38, v167
	v_add_u32_e32 v154, s39, v167
	ds_read_b128 v[122:125], v134
	ds_read_b128 v[126:129], v134 offset:1024
	ds_read_b128 v[130:133], v134 offset:2048
	ds_read_b128 v[134:137], v134 offset:3072
	ds_read_b128 v[172:175], v154
	ds_read_b128 v[176:179], v154 offset:1024
	ds_read_b128 v[180:183], v154 offset:2048
	ds_read_b128 v[184:187], v154 offset:3072
	s_add_u32 s28, s28, 0x80000
	s_addc_u32 s29, s29, 0
	s_mov_b32 m0, s36
	ds_read_b128 v[188:191], v171 offset:32768
	ds_read_b128 v[192:195], v171 offset:33792
	ds_read_b128 v[196:199], v171 offset:34816
	ds_read_b128 v[200:203], v171 offset:35840
	ds_read_b128 v[204:207], v171 offset:36864
	ds_read_b128 v[208:211], v171 offset:37888
	ds_read_b128 v[212:215], v171 offset:38912
	ds_read_b128 v[216:219], v171 offset:39936
	global_load_lds_dwordx4 v146, s[28:29]
	s_mov_b32 m0, s37
	s_nop 0
	global_load_lds_dwordx4 v150, s[28:29]
	s_waitcnt vmcnt(8)
	s_waitcnt lgkmcnt(0)
	s_barrier
	s_waitcnt lgkmcnt(0)
	v_mfma_i32_16x16x64_i8 v[142:145], v[122:125], v[188:191], v[142:145]
	v_mfma_i32_16x16x64_i8 v[138:141], v[130:133], v[188:191], v[138:141]
	v_mfma_i32_16x16x64_i8 v[110:113], v[122:125], v[196:199], v[110:113]
	v_mfma_i32_16x16x64_i8 v[106:109], v[130:133], v[196:199], v[106:109]
	v_mfma_i32_16x16x64_i8 v[94:97], v[122:125], v[204:207], v[94:97]
	v_mfma_i32_16x16x64_i8 v[90:93], v[130:133], v[204:207], v[90:93]
	v_mfma_i32_16x16x64_i8 v[78:81], v[122:125], v[212:215], v[78:81]
	v_mfma_i32_16x16x64_i8 v[74:77], v[130:133], v[212:215], v[74:77]
	v_mfma_i32_16x16x64_i8 v[142:145], v[126:129], v[192:195], v[142:145]
	v_mfma_i32_16x16x64_i8 v[138:141], v[134:137], v[192:195], v[138:141]
	v_mfma_i32_16x16x64_i8 v[110:113], v[126:129], v[200:203], v[110:113]
	v_mfma_i32_16x16x64_i8 v[106:109], v[134:137], v[200:203], v[106:109]
	v_mfma_i32_16x16x64_i8 v[94:97], v[126:129], v[208:211], v[94:97]
	v_mfma_i32_16x16x64_i8 v[90:93], v[134:137], v[208:211], v[90:93]
	v_mfma_i32_16x16x64_i8 v[78:81], v[126:129], v[216:219], v[78:81]
	v_mfma_i32_16x16x64_i8 v[74:77], v[134:137], v[216:219], v[74:77]
	v_mfma_i32_16x16x64_i8 v[118:121], v[172:175], v[188:191], v[118:121]
	v_mfma_i32_16x16x64_i8 v[114:117], v[180:183], v[188:191], v[114:117]
	v_mfma_i32_16x16x64_i8 v[102:105], v[172:175], v[196:199], v[102:105]
	v_mfma_i32_16x16x64_i8 v[98:101], v[180:183], v[196:199], v[98:101]
	v_mfma_i32_16x16x64_i8 v[86:89], v[172:175], v[204:207], v[86:89]
	v_mfma_i32_16x16x64_i8 v[82:85], v[180:183], v[204:207], v[82:85]
	v_mfma_i32_16x16x64_i8 v[70:73], v[172:175], v[212:215], v[70:73]
	v_mfma_i32_16x16x64_i8 v[66:69], v[180:183], v[212:215], v[66:69]
	v_mfma_i32_16x16x64_i8 v[118:121], v[176:179], v[192:195], v[118:121]
	v_mfma_i32_16x16x64_i8 v[114:117], v[184:187], v[192:195], v[114:117]
	v_mfma_i32_16x16x64_i8 v[102:105], v[176:179], v[200:203], v[102:105]
	v_mfma_i32_16x16x64_i8 v[98:101], v[184:187], v[200:203], v[98:101]
	v_mfma_i32_16x16x64_i8 v[86:89], v[176:179], v[208:211], v[86:89]
	v_mfma_i32_16x16x64_i8 v[82:85], v[184:187], v[208:211], v[82:85]
	v_mfma_i32_16x16x64_i8 v[70:73], v[176:179], v[216:219], v[70:73]
	v_mfma_i32_16x16x64_i8 v[66:69], v[184:187], v[216:219], v[66:69]
	s_barrier
	s_add_i32 s28, s38, s34
	s_mov_b32 m0, s28
	ds_read_b128 v[188:191], v171 offset:49152
	ds_read_b128 v[192:195], v171 offset:50176
	ds_read_b128 v[196:199], v171 offset:51200
	ds_read_b128 v[200:203], v171 offset:52224
	ds_read_b128 v[204:207], v171 offset:53248
	ds_read_b128 v[208:211], v171 offset:54272
	ds_read_b128 v[212:215], v171 offset:55296
	ds_read_b128 v[216:219], v171 offset:56320
	global_load_lds_dwordx4 v148, s[98:99]
	s_add_i32 m0, s28, 0x2000
	s_add_u32 s26, s26, 0x80080
	s_addc_u32 s27, s27, 0
	s_add_i32 s28, s39, s34
	global_load_lds_dwordx4 v152, s[98:99]
	s_mov_b32 m0, s28
	s_nop 0
	global_load_lds_dwordx4 v148, s[26:27]
	s_add_i32 m0, s28, 0x2000
	s_nop 0
	global_load_lds_dwordx4 v152, s[26:27]
	s_mov_b32 m0, s43
	s_nop 0
	global_load_lds_dwordx4 v146, s[100:101]
	s_mov_b32 m0, s44
	s_nop 0
	global_load_lds_dwordx4 v150, s[100:101]
	s_waitcnt vmcnt(8)
	s_waitcnt lgkmcnt(0)
	s_barrier
	s_waitcnt lgkmcnt(0)
	v_mfma_i32_16x16x64_i8 v[62:65], v[122:125], v[188:191], v[62:65]
	v_mfma_i32_16x16x64_i8 v[58:61], v[130:133], v[188:191], v[58:61]
	v_mfma_i32_16x16x64_i8 v[46:49], v[122:125], v[196:199], v[46:49]
	v_mfma_i32_16x16x64_i8 v[42:45], v[130:133], v[196:199], v[42:45]
	v_mfma_i32_16x16x64_i8 v[30:33], v[122:125], v[204:207], v[30:33]
	v_mfma_i32_16x16x64_i8 v[26:29], v[130:133], v[204:207], v[26:29]
	v_mfma_i32_16x16x64_i8 v[14:17], v[122:125], v[212:215], v[14:17]
	v_mfma_i32_16x16x64_i8 v[10:13], v[130:133], v[212:215], v[10:13]
	v_mfma_i32_16x16x64_i8 v[62:65], v[126:129], v[192:195], v[62:65]
	v_mfma_i32_16x16x64_i8 v[58:61], v[134:137], v[192:195], v[58:61]
	v_mfma_i32_16x16x64_i8 v[46:49], v[126:129], v[200:203], v[46:49]
	v_mfma_i32_16x16x64_i8 v[42:45], v[134:137], v[200:203], v[42:45]
	v_mfma_i32_16x16x64_i8 v[30:33], v[126:129], v[208:211], v[30:33]
	v_mfma_i32_16x16x64_i8 v[26:29], v[134:137], v[208:211], v[26:29]
	v_mfma_i32_16x16x64_i8 v[14:17], v[126:129], v[216:219], v[14:17]
	v_mfma_i32_16x16x64_i8 v[10:13], v[134:137], v[216:219], v[10:13]
	v_mfma_i32_16x16x64_i8 v[54:57], v[172:175], v[188:191], v[54:57]
	v_mfma_i32_16x16x64_i8 v[50:53], v[180:183], v[188:191], v[50:53]
	v_mfma_i32_16x16x64_i8 v[38:41], v[172:175], v[196:199], v[38:41]
	v_mfma_i32_16x16x64_i8 v[34:37], v[180:183], v[196:199], v[34:37]
	v_mfma_i32_16x16x64_i8 v[22:25], v[172:175], v[204:207], v[22:25]
	v_mfma_i32_16x16x64_i8 v[18:21], v[180:183], v[204:207], v[18:21]
	v_mfma_i32_16x16x64_i8 v[6:9], v[172:175], v[212:215], v[6:9]
	v_mfma_i32_16x16x64_i8 v[2:5], v[180:183], v[212:215], v[2:5]
	v_mfma_i32_16x16x64_i8 v[54:57], v[176:179], v[192:195], v[54:57]
	v_mfma_i32_16x16x64_i8 v[50:53], v[184:187], v[192:195], v[50:53]
	v_mfma_i32_16x16x64_i8 v[38:41], v[176:179], v[200:203], v[38:41]
	v_mfma_i32_16x16x64_i8 v[34:37], v[184:187], v[200:203], v[34:37]
	v_mfma_i32_16x16x64_i8 v[22:25], v[176:179], v[208:211], v[22:25]
	v_mfma_i32_16x16x64_i8 v[18:21], v[184:187], v[208:211], v[18:21]
	v_mfma_i32_16x16x64_i8 v[6:9], v[176:179], v[216:219], v[6:9]
	v_mfma_i32_16x16x64_i8 v[2:5], v[184:187], v[216:219], v[2:5]
	s_barrier
	s_add_i32 s53, s53, 2
	s_add_u32 s24, s24, 0x100
	s_addc_u32 s25, s25, 0
	s_add_u32 s51, s51, 0x100
	s_addc_u32 s52, s52, 0
	s_cmp_gt_u32 s53, 29
	s_cbranch_scc0 .LBB0_1489
	s_and_b64 vcc, exec, s[12:13]
	s_cbranch_vccz .LBB0_1492
	s_barrier

.LBB0_1550:
	s_setprio 0
	s_cmp_lt_i32 s70, 8
	s_cselect_b64 s[0:1], -1, 0
	s_and_b64 s[6:7], s[0:1], s[2:3]
	s_andn2_b64 vcc, exec, s[6:7]
	s_cbranch_vccnz .LBB0_1575
	v_readlane_b32 s8, v254, 51
	v_readlane_b32 s9, v254, 52
	v_readlane_b32 s16, v254, 59
	v_readlane_b32 s17, v254, 60
	s_mov_b64 s[8:9], s[16:17]
	s_add_u32 s0, s8, 0x4000
	s_addc_u32 s1, s9, 0
	s_add_u32 s2, s8, 0x8000
	s_addc_u32 s3, s9, 0
	s_mov_b64 s[4:5], 0
	v_mov_b32_e32 v3, 0
	s_movk_i32 s8, 0x5ff
	v_mov_b32_e32 v1, v0
	v_readlane_b32 s10, v254, 53
	v_readlane_b32 s11, v254, 54
	v_readlane_b32 s12, v254, 55
	v_readlane_b32 s13, v254, 56
	v_readlane_b32 s14, v254, 57
	v_readlane_b32 s15, v254, 58
	v_readlane_b32 s18, v254, 61
	v_readlane_b32 s19, v254, 62
	v_readlane_b32 s20, v254, 63
	v_readlane_b32 s21, v255, 0
	v_readlane_b32 s22, v255, 1
	v_readlane_b32 s23, v255, 2

.Lprio_P8:
.LBB0_1649:
	ds_read_b128 v[130:133], v167
	ds_read_b128 v[134:137], v167 offset:1024
	ds_read_b128 v[138:141], v167 offset:2048
	ds_read_b128 v[142:145], v167 offset:3072
	ds_read_b128 v[168:171], v228
	ds_read_b128 v[172:175], v228 offset:1024
	ds_read_b128 v[176:179], v228 offset:2048
	ds_read_b128 v[180:183], v228 offset:3072
	s_add_u32 s38, s34, 0xfff80080
	s_addc_u32 s39, s35, -1
	s_cmp_eq_u32 s77, 28
	s_cselect_b32 s45, s1, s39
	s_cselect_b32 s44, s29, s38
	s_cselect_b32 s43, s27, s47
	s_cselect_b32 s42, s41, s46
	s_add_i32 m0, s50, 0xc000
	ds_read_b128 v[184:187], v229
	ds_read_b128 v[188:191], v229 offset:1024
	ds_read_b128 v[192:195], v229 offset:2048
	ds_read_b128 v[196:199], v229 offset:3072
	ds_read_b128 v[200:203], v229 offset:4096
	ds_read_b128 v[204:207], v229 offset:5120
	ds_read_b128 v[208:211], v229 offset:6144
	ds_read_b128 v[212:215], v229 offset:7168
	global_load_lds_dwordx4 v158, s[34:35]
	s_add_i32 m0, s50, 0xe000
	s_nop 0
	global_load_lds_dwordx4 v160, s[34:35]
	s_waitcnt vmcnt(8)
	s_waitcnt lgkmcnt(0)
	s_barrier
	s_waitcnt lgkmcnt(0)
	v_mfma_i32_16x16x64_i8 v[46:49], v[130:133], v[184:187], v[46:49]
	v_mfma_i32_16x16x64_i8 v[34:37], v[138:141], v[184:187], v[34:37]
	v_mfma_i32_16x16x64_i8 v[42:45], v[130:133], v[192:195], v[42:45]
	v_mfma_i32_16x16x64_i8 v[30:33], v[138:141], v[192:195], v[30:33]
	v_mfma_i32_16x16x64_i8 v[38:41], v[130:133], v[200:203], v[38:41]
	v_mfma_i32_16x16x64_i8 v[26:29], v[138:141], v[200:203], v[26:29]
	v_mfma_i32_16x16x64_i8 v[126:129], v[130:133], v[208:211], v[126:129]
	v_mfma_i32_16x16x64_i8 v[122:125], v[138:141], v[208:211], v[122:125]
	v_mfma_i32_16x16x64_i8 v[46:49], v[134:137], v[188:191], v[46:49]
	v_mfma_i32_16x16x64_i8 v[34:37], v[142:145], v[188:191], v[34:37]
	v_mfma_i32_16x16x64_i8 v[42:45], v[134:137], v[196:199], v[42:45]
	v_mfma_i32_16x16x64_i8 v[30:33], v[142:145], v[196:199], v[30:33]
	v_mfma_i32_16x16x64_i8 v[38:41], v[134:137], v[204:207], v[38:41]
	v_mfma_i32_16x16x64_i8 v[26:29], v[142:145], v[204:207], v[26:29]
	v_mfma_i32_16x16x64_i8 v[126:129], v[134:137], v[212:215], v[126:129]
	v_mfma_i32_16x16x64_i8 v[122:125], v[142:145], v[212:215], v[122:125]
	v_mfma_i32_16x16x64_i8 v[22:25], v[168:171], v[184:187], v[22:25]
	v_mfma_i32_16x16x64_i8 v[10:13], v[176:179], v[184:187], v[10:13]
	v_mfma_i32_16x16x64_i8 v[18:21], v[168:171], v[192:195], v[18:21]
	v_mfma_i32_16x16x64_i8 v[6:9], v[176:179], v[192:195], v[6:9]
	v_mfma_i32_16x16x64_i8 v[14:17], v[168:171], v[200:203], v[14:17]
	v_mfma_i32_16x16x64_i8 v[2:5], v[176:179], v[200:203], v[2:5]
	v_mfma_i32_16x16x64_i8 v[118:121], v[168:171], v[208:211], v[118:121]
	v_mfma_i32_16x16x64_i8 v[114:117], v[176:179], v[208:211], v[114:117]
	v_mfma_i32_16x16x64_i8 v[22:25], v[172:175], v[188:191], v[22:25]
	v_mfma_i32_16x16x64_i8 v[10:13], v[180:183], v[188:191], v[10:13]
	v_mfma_i32_16x16x64_i8 v[18:21], v[172:175], v[196:199], v[18:21]
	v_mfma_i32_16x16x64_i8 v[6:9], v[180:183], v[196:199], v[6:9]
	v_mfma_i32_16x16x64_i8 v[14:17], v[172:175], v[204:207], v[14:17]
	v_mfma_i32_16x16x64_i8 v[2:5], v[180:183], v[204:207], v[2:5]
	v_mfma_i32_16x16x64_i8 v[118:121], v[172:175], v[212:215], v[118:121]
	v_mfma_i32_16x16x64_i8 v[114:117], v[180:183], v[212:215], v[114:117]
	s_barrier
	s_add_u32 s98, s42, s14
	s_addc_u32 s99, s43, s15
	s_add_u32 s100, s44, s14
	s_addc_u32 s101, s45, s15
	s_add_i32 s38, s64, s49
	s_mov_b32 m0, s38
	ds_read_b128 v[184:187], v229 offset:16384
	ds_read_b128 v[188:191], v229 offset:17408
	ds_read_b128 v[192:195], v229 offset:18432
	ds_read_b128 v[196:199], v229 offset:19456
	ds_read_b128 v[200:203], v229 offset:20480
	ds_read_b128 v[204:207], v229 offset:21504
	ds_read_b128 v[208:211], v229 offset:22528
	ds_read_b128 v[212:215], v229 offset:23552
	global_load_lds_dwordx4 v150, s[42:43]
	s_add_i32 m0, s38, 0x2000
	s_add_u32 s38, s42, 0x80000
	s_addc_u32 s39, s43, 0
	s_add_i32 s78, s65, s49
	global_load_lds_dwordx4 v154, s[42:43]
	s_mov_b32 m0, s78
	s_nop 0
	global_load_lds_dwordx4 v150, s[38:39]
	s_add_i32 m0, s78, 0x2000
	s_nop 0
	global_load_lds_dwordx4 v154, s[38:39]
	s_mov_b32 m0, s50
	s_nop 0
	global_load_lds_dwordx4 v148, s[44:45]
	s_mov_b32 m0, s51
	s_nop 0
	global_load_lds_dwordx4 v152, s[44:45]
	s_waitcnt vmcnt(8)
	s_waitcnt lgkmcnt(0)
	s_barrier
	s_waitcnt lgkmcnt(0)
	v_mfma_i32_16x16x64_i8 v[94:97], v[130:133], v[184:187], v[94:97]
	v_mfma_i32_16x16x64_i8 v[70:73], v[138:141], v[184:187], v[70:73]
	v_mfma_i32_16x16x64_i8 v[86:89], v[130:133], v[192:195], v[86:89]
	v_mfma_i32_16x16x64_i8 v[62:65], v[138:141], v[192:195], v[62:65]
	v_mfma_i32_16x16x64_i8 v[78:81], v[130:133], v[200:203], v[78:81]
	v_mfma_i32_16x16x64_i8 v[54:57], v[138:141], v[200:203], v[54:57]
	v_mfma_i32_16x16x64_i8 v[110:113], v[130:133], v[208:211], v[110:113]
	v_mfma_i32_16x16x64_i8 v[106:109], v[138:141], v[208:211], v[106:109]
	v_mfma_i32_16x16x64_i8 v[94:97], v[134:137], v[188:191], v[94:97]
	v_mfma_i32_16x16x64_i8 v[70:73], v[142:145], v[188:191], v[70:73]
	v_mfma_i32_16x16x64_i8 v[86:89], v[134:137], v[196:199], v[86:89]
	v_mfma_i32_16x16x64_i8 v[62:65], v[142:145], v[196:199], v[62:65]
	v_mfma_i32_16x16x64_i8 v[78:81], v[134:137], v[204:207], v[78:81]
	v_mfma_i32_16x16x64_i8 v[54:57], v[142:145], v[204:207], v[54:57]
	v_mfma_i32_16x16x64_i8 v[110:113], v[134:137], v[212:215], v[110:113]
	v_mfma_i32_16x16x64_i8 v[106:109], v[142:145], v[212:215], v[106:109]
	v_mfma_i32_16x16x64_i8 v[90:93], v[168:171], v[184:187], v[90:93]
	v_mfma_i32_16x16x64_i8 v[66:69], v[176:179], v[184:187], v[66:69]
	v_mfma_i32_16x16x64_i8 v[82:85], v[168:171], v[192:195], v[82:85]
	v_mfma_i32_16x16x64_i8 v[58:61], v[176:179], v[192:195], v[58:61]
	v_mfma_i32_16x16x64_i8 v[74:77], v[168:171], v[200:203], v[74:77]
	v_mfma_i32_16x16x64_i8 v[50:53], v[176:179], v[200:203], v[50:53]
	v_mfma_i32_16x16x64_i8 v[102:105], v[168:171], v[208:211], v[102:105]
	v_mfma_i32_16x16x64_i8 v[98:101], v[176:179], v[208:211], v[98:101]
	v_mfma_i32_16x16x64_i8 v[90:93], v[172:175], v[188:191], v[90:93]
	v_mfma_i32_16x16x64_i8 v[66:69], v[180:183], v[188:191], v[66:69]
	v_mfma_i32_16x16x64_i8 v[82:85], v[172:175], v[196:199], v[82:85]
	v_mfma_i32_16x16x64_i8 v[58:61], v[180:183], v[196:199], v[58:61]
	v_mfma_i32_16x16x64_i8 v[74:77], v[172:175], v[204:207], v[74:77]
	v_mfma_i32_16x16x64_i8 v[50:53], v[180:183], v[204:207], v[50:53]
	v_mfma_i32_16x16x64_i8 v[102:105], v[172:175], v[212:215], v[102:105]
	v_mfma_i32_16x16x64_i8 v[98:101], v[180:183], v[212:215], v[98:101]
	s_barrier
	s_add_i32 s78, 0, 0x18000
	s_add_i32 s79, 0, 0x1c000
	v_add_u32_e32 v142, s78, v1
	v_add_u32_e32 v156, s79, v1
	ds_read_b128 v[130:133], v142
	ds_read_b128 v[134:137], v142 offset:1024
	ds_read_b128 v[138:141], v142 offset:2048
	ds_read_b128 v[142:145], v142 offset:3072
	ds_read_b128 v[168:171], v156
	ds_read_b128 v[172:175], v156 offset:1024
	ds_read_b128 v[176:179], v156 offset:2048
	ds_read_b128 v[180:183], v156 offset:3072
	s_add_u32 s38, s44, 0x80000
	s_addc_u32 s39, s45, 0
	s_mov_b32 m0, s52
	ds_read_b128 v[184:187], v229 offset:32768
	ds_read_b128 v[188:191], v229 offset:33792
	ds_read_b128 v[192:195], v229 offset:34816
	ds_read_b128 v[196:199], v229 offset:35840
	ds_read_b128 v[200:203], v229 offset:36864
	ds_read_b128 v[204:207], v229 offset:37888
	ds_read_b128 v[208:211], v229 offset:38912
	ds_read_b128 v[212:215], v229 offset:39936
	global_load_lds_dwordx4 v148, s[38:39]
	s_mov_b32 m0, s53
	s_nop 0
	global_load_lds_dwordx4 v152, s[38:39]
	s_waitcnt vmcnt(8)
	s_waitcnt lgkmcnt(0)
	s_barrier
	s_waitcnt lgkmcnt(0)
	v_mfma_i32_16x16x64_i8 v[46:49], v[130:133], v[184:187], v[46:49]
	v_mfma_i32_16x16x64_i8 v[34:37], v[138:141], v[184:187], v[34:37]
	v_mfma_i32_16x16x64_i8 v[42:45], v[130:133], v[192:195], v[42:45]
	v_mfma_i32_16x16x64_i8 v[30:33], v[138:141], v[192:195], v[30:33]
	v_mfma_i32_16x16x64_i8 v[38:41], v[130:133], v[200:203], v[38:41]
	v_mfma_i32_16x16x64_i8 v[26:29], v[138:141], v[200:203], v[26:29]
	v_mfma_i32_16x16x64_i8 v[126:129], v[130:133], v[208:211], v[126:129]
	v_mfma_i32_16x16x64_i8 v[122:125], v[138:141], v[208:211], v[122:125]
	v_mfma_i32_16x16x64_i8 v[46:49], v[134:137], v[188:191], v[46:49]
	v_mfma_i32_16x16x64_i8 v[34:37], v[142:145], v[188:191], v[34:37]
	v_mfma_i32_16x16x64_i8 v[42:45], v[134:137], v[196:199], v[42:45]
	v_mfma_i32_16x16x64_i8 v[30:33], v[142:145], v[196:199], v[30:33]
	v_mfma_i32_16x16x64_i8 v[38:41], v[134:137], v[204:207], v[38:41]
	v_mfma_i32_16x16x64_i8 v[26:29], v[142:145], v[204:207], v[26:29]
	v_mfma_i32_16x16x64_i8 v[126:129], v[134:137], v[212:215], v[126:129]
	v_mfma_i32_16x16x64_i8 v[122:125], v[142:145], v[212:215], v[122:125]
	v_mfma_i32_16x16x64_i8 v[22:25], v[168:171], v[184:187], v[22:25]
	v_mfma_i32_16x16x64_i8 v[10:13], v[176:179], v[184:187], v[10:13]
	v_mfma_i32_16x16x64_i8 v[18:21], v[168:171], v[192:195], v[18:21]
	v_mfma_i32_16x16x64_i8 v[6:9], v[176:179], v[192:195], v[6:9]
	v_mfma_i32_16x16x64_i8 v[14:17], v[168:171], v[200:203], v[14:17]
	v_mfma_i32_16x16x64_i8 v[2:5], v[176:179], v[200:203], v[2:5]
	v_mfma_i32_16x16x64_i8 v[118:121], v[168:171], v[208:211], v[118:121]
	v_mfma_i32_16x16x64_i8 v[114:117], v[176:179], v[208:211], v[114:117]
	v_mfma_i32_16x16x64_i8 v[22:25], v[172:175], v[188:191], v[22:25]
	v_mfma_i32_16x16x64_i8 v[10:13], v[180:183], v[188:191], v[10:13]
	v_mfma_i32_16x16x64_i8 v[18:21], v[172:175], v[196:199], v[18:21]
	v_mfma_i32_16x16x64_i8 v[6:9], v[180:183], v[196:199], v[6:9]
	v_mfma_i32_16x16x64_i8 v[14:17], v[172:175], v[204:207], v[14:17]
	v_mfma_i32_16x16x64_i8 v[2:5], v[180:183], v[204:207], v[2:5]
	v_mfma_i32_16x16x64_i8 v[118:121], v[172:175], v[212:215], v[118:121]
	v_mfma_i32_16x16x64_i8 v[114:117], v[180:183], v[212:215], v[114:117]
	s_barrier
	s_add_i32 s38, s78, s49
	s_mov_b32 m0, s38
	ds_read_b128 v[184:187], v229 offset:49152
	ds_read_b128 v[188:191], v229 offset:50176
	ds_read_b128 v[192:195], v229 offset:51200
	ds_read_b128 v[196:199], v229 offset:52224
	ds_read_b128 v[200:203], v229 offset:53248
	ds_read_b128 v[204:207], v229 offset:54272
	ds_read_b128 v[208:211], v229 offset:55296
	ds_read_b128 v[212:215], v229 offset:56320
	global_load_lds_dwordx4 v150, s[98:99]
	s_add_i32 m0, s38, 0x2000
	s_add_u32 s38, s42, 0x80080
	s_addc_u32 s39, s43, 0
	s_add_i32 s42, s79, s49
	global_load_lds_dwordx4 v154, s[98:99]
	s_mov_b32 m0, s42
	s_nop 0
	global_load_lds_dwordx4 v150, s[38:39]
	s_add_i32 m0, s42, 0x2000
	s_nop 0
	global_load_lds_dwordx4 v154, s[38:39]
	s_mov_b32 m0, s57
	s_nop 0
	global_load_lds_dwordx4 v148, s[100:101]
	s_mov_b32 m0, s58
	s_nop 0
	global_load_lds_dwordx4 v152, s[100:101]
	s_waitcnt vmcnt(8)
	s_waitcnt lgkmcnt(0)
	s_barrier
	s_waitcnt lgkmcnt(0)
	v_mfma_i32_16x16x64_i8 v[94:97], v[130:133], v[184:187], v[94:97]
	v_mfma_i32_16x16x64_i8 v[70:73], v[138:141], v[184:187], v[70:73]
	v_mfma_i32_16x16x64_i8 v[86:89], v[130:133], v[192:195], v[86:89]
	v_mfma_i32_16x16x64_i8 v[62:65], v[138:141], v[192:195], v[62:65]
	v_mfma_i32_16x16x64_i8 v[78:81], v[130:133], v[200:203], v[78:81]
	v_mfma_i32_16x16x64_i8 v[54:57], v[138:141], v[200:203], v[54:57]
	v_mfma_i32_16x16x64_i8 v[110:113], v[130:133], v[208:211], v[110:113]
	v_mfma_i32_16x16x64_i8 v[106:109], v[138:141], v[208:211], v[106:109]
	v_mfma_i32_16x16x64_i8 v[94:97], v[134:137], v[188:191], v[94:97]
	v_mfma_i32_16x16x64_i8 v[70:73], v[142:145], v[188:191], v[70:73]
	v_mfma_i32_16x16x64_i8 v[86:89], v[134:137], v[196:199], v[86:89]
	v_mfma_i32_16x16x64_i8 v[62:65], v[142:145], v[196:199], v[62:65]
	v_mfma_i32_16x16x64_i8 v[78:81], v[134:137], v[204:207], v[78:81]
	v_mfma_i32_16x16x64_i8 v[54:57], v[142:145], v[204:207], v[54:57]
	v_mfma_i32_16x16x64_i8 v[110:113], v[134:137], v[212:215], v[110:113]
	v_mfma_i32_16x16x64_i8 v[106:109], v[142:145], v[212:215], v[106:109]
	v_mfma_i32_16x16x64_i8 v[90:93], v[168:171], v[184:187], v[90:93]
	v_mfma_i32_16x16x64_i8 v[66:69], v[176:179], v[184:187], v[66:69]
	v_mfma_i32_16x16x64_i8 v[82:85], v[168:171], v[192:195], v[82:85]
	v_mfma_i32_16x16x64_i8 v[58:61], v[176:179], v[192:195], v[58:61]
	v_mfma_i32_16x16x64_i8 v[74:77], v[168:171], v[200:203], v[74:77]
	v_mfma_i32_16x16x64_i8 v[50:53], v[176:179], v[200:203], v[50:53]
	v_mfma_i32_16x16x64_i8 v[102:105], v[168:171], v[208:211], v[102:105]
	v_mfma_i32_16x16x64_i8 v[98:101], v[176:179], v[208:211], v[98:101]
	v_mfma_i32_16x16x64_i8 v[90:93], v[172:175], v[188:191], v[90:93]
	v_mfma_i32_16x16x64_i8 v[66:69], v[180:183], v[188:191], v[66:69]
	v_mfma_i32_16x16x64_i8 v[82:85], v[172:175], v[196:199], v[82:85]
	v_mfma_i32_16x16x64_i8 v[58:61], v[180:183], v[196:199], v[58:61]
	v_mfma_i32_16x16x64_i8 v[74:77], v[172:175], v[204:207], v[74:77]
	v_mfma_i32_16x16x64_i8 v[50:53], v[180:183], v[204:207], v[50:53]
	v_mfma_i32_16x16x64_i8 v[102:105], v[172:175], v[212:215], v[102:105]
	v_mfma_i32_16x16x64_i8 v[98:101], v[180:183], v[212:215], v[98:101]
	s_barrier
	s_add_i32 s77, s77, 2
	s_add_u32 s34, s34, 0x100
	s_addc_u32 s35, s35, 0
	s_add_u32 s46, s46, 0x100
	s_addc_u32 s47, s47, 0
	s_cmp_gt_u32 s77, 29
	s_cbranch_scc0 .LBB0_1649
	s_and_b64 vcc, exec, s[16:17]
	s_cbranch_vccz .LBB0_1652
	s_barrier

.LBB0_1750:
	s_setprio 0
	s_cmp_lt_i32 s70, 10
	s_cselect_b64 s[2:3], -1, 0
	s_and_b64 s[14:15], s[2:3], s[0:1]
	s_andn2_b64 vcc, exec, s[14:15]
	s_cbranch_vccnz .LBB0_1823
	v_lshl_or_b32 v1, s90, 9, v0
	s_mov_b32 s0, 0x15800
	v_cmp_gt_i32_e32 vcc, s0, v1
	s_and_saveexec_b64 s[0:1], vcc
	s_cbranch_execz .LBB0_1762
	s_lshl_b32 s20, s91, 9
	s_add_u32 s10, s80, 0x15800
	s_addc_u32 s11, s81, 0
	s_add_u32 s12, s80, 0x2b000
	s_addc_u32 s13, s81, 0
	v_lshlrev_b32_e32 v134, 3, v1
	s_lshl_b32 s21, s91, 12
	s_mov_b64 s[16:17], 0
	s_mov_b32 s22, 0x2fa0be83
	s_mov_b32 s23, 0xac00
	s_movk_i32 s24, 0x5600
	s_mov_b32 s25, 0x157ff
	s_branch .LBB0_1754

.Lprio_P10:
.LBB0_1899:
	ds_read_b128 v[122:125], v169
	ds_read_b128 v[126:129], v169 offset:1024
	ds_read_b128 v[130:133], v169 offset:2048
	ds_read_b128 v[134:137], v169 offset:3072
	ds_read_b128 v[172:175], v170
	ds_read_b128 v[176:179], v170 offset:1024
	ds_read_b128 v[180:183], v170 offset:2048
	ds_read_b128 v[184:187], v170 offset:3072
	s_add_u32 s22, s20, 0xffea8080
	s_addc_u32 s23, s21, -1
	s_cmpk_eq_i32 s49, 0x52
	s_cselect_b32 s25, s5, s23
	s_cselect_b32 s24, s4, s22
	s_cselect_b32 s23, s19, s48
	s_cselect_b32 s22, s18, s47
	s_add_i32 m0, s30, 0xc000
	ds_read_b128 v[188:191], v171
	ds_read_b128 v[192:195], v171 offset:1024
	ds_read_b128 v[196:199], v171 offset:2048
	ds_read_b128 v[200:203], v171 offset:3072
	ds_read_b128 v[204:207], v171 offset:4096
	ds_read_b128 v[208:211], v171 offset:5120
	ds_read_b128 v[212:215], v171 offset:6144
	ds_read_b128 v[216:219], v171 offset:7168
	global_load_lds_dwordx4 v156, s[20:21]
	s_add_i32 m0, s30, 0xe000
	s_nop 0
	global_load_lds_dwordx4 v158, s[20:21]
	s_waitcnt vmcnt(8)
	s_waitcnt lgkmcnt(0)
	s_barrier
	s_waitcnt lgkmcnt(0)
	v_mfma_i32_16x16x64_i8 v[142:145], v[122:125], v[188:191], v[142:145]
	v_mfma_i32_16x16x64_i8 v[138:141], v[130:133], v[188:191], v[138:141]
	v_mfma_i32_16x16x64_i8 v[110:113], v[122:125], v[196:199], v[110:113]
	v_mfma_i32_16x16x64_i8 v[106:109], v[130:133], v[196:199], v[106:109]
	v_mfma_i32_16x16x64_i8 v[94:97], v[122:125], v[204:207], v[94:97]
	v_mfma_i32_16x16x64_i8 v[90:93], v[130:133], v[204:207], v[90:93]
	v_mfma_i32_16x16x64_i8 v[78:81], v[122:125], v[212:215], v[78:81]
	v_mfma_i32_16x16x64_i8 v[74:77], v[130:133], v[212:215], v[74:77]
	v_mfma_i32_16x16x64_i8 v[142:145], v[126:129], v[192:195], v[142:145]
	v_mfma_i32_16x16x64_i8 v[138:141], v[134:137], v[192:195], v[138:141]
	v_mfma_i32_16x16x64_i8 v[110:113], v[126:129], v[200:203], v[110:113]
	v_mfma_i32_16x16x64_i8 v[106:109], v[134:137], v[200:203], v[106:109]
	v_mfma_i32_16x16x64_i8 v[94:97], v[126:129], v[208:211], v[94:97]
	v_mfma_i32_16x16x64_i8 v[90:93], v[134:137], v[208:211], v[90:93]
	v_mfma_i32_16x16x64_i8 v[78:81], v[126:129], v[216:219], v[78:81]
	v_mfma_i32_16x16x64_i8 v[74:77], v[134:137], v[216:219], v[74:77]
	v_mfma_i32_16x16x64_i8 v[118:121], v[172:175], v[188:191], v[118:121]
	v_mfma_i32_16x16x64_i8 v[114:117], v[180:183], v[188:191], v[114:117]
	v_mfma_i32_16x16x64_i8 v[102:105], v[172:175], v[196:199], v[102:105]
	v_mfma_i32_16x16x64_i8 v[98:101], v[180:183], v[196:199], v[98:101]
	v_mfma_i32_16x16x64_i8 v[86:89], v[172:175], v[204:207], v[86:89]
	v_mfma_i32_16x16x64_i8 v[82:85], v[180:183], v[204:207], v[82:85]
	v_mfma_i32_16x16x64_i8 v[70:73], v[172:175], v[212:215], v[70:73]
	v_mfma_i32_16x16x64_i8 v[66:69], v[180:183], v[212:215], v[66:69]
	v_mfma_i32_16x16x64_i8 v[118:121], v[176:179], v[192:195], v[118:121]
	v_mfma_i32_16x16x64_i8 v[114:117], v[184:187], v[192:195], v[114:117]
	v_mfma_i32_16x16x64_i8 v[102:105], v[176:179], v[200:203], v[102:105]
	v_mfma_i32_16x16x64_i8 v[98:101], v[184:187], v[200:203], v[98:101]
	v_mfma_i32_16x16x64_i8 v[86:89], v[176:179], v[208:211], v[86:89]
	v_mfma_i32_16x16x64_i8 v[82:85], v[184:187], v[208:211], v[82:85]
	v_mfma_i32_16x16x64_i8 v[70:73], v[176:179], v[216:219], v[70:73]
	v_mfma_i32_16x16x64_i8 v[66:69], v[184:187], v[216:219], v[66:69]
	s_barrier
	s_add_u32 s98, s22, s14
	s_addc_u32 s99, s23, s15
	s_add_u32 s100, s24, s14
	s_addc_u32 s101, s25, s15
	s_add_i32 s38, s41, s29
	s_mov_b32 m0, s38
	ds_read_b128 v[188:191], v171 offset:16384
	ds_read_b128 v[192:195], v171 offset:17408
	ds_read_b128 v[196:199], v171 offset:18432
	ds_read_b128 v[200:203], v171 offset:19456
	ds_read_b128 v[204:207], v171 offset:20480
	ds_read_b128 v[208:211], v171 offset:21504
	ds_read_b128 v[212:215], v171 offset:22528
	ds_read_b128 v[216:219], v171 offset:23552
	global_load_lds_dwordx4 v148, s[22:23]
	s_add_i32 m0, s38, 0x2000
	s_add_u32 s38, s22, 0x158000
	s_addc_u32 s39, s23, 0
	s_add_i32 s50, s42, s29
	global_load_lds_dwordx4 v152, s[22:23]
	s_mov_b32 m0, s50
	s_nop 0
	global_load_lds_dwordx4 v148, s[38:39]
	s_add_i32 m0, s50, 0x2000
	s_nop 0
	global_load_lds_dwordx4 v152, s[38:39]
	s_mov_b32 m0, s30
	s_nop 0
	global_load_lds_dwordx4 v146, s[24:25]
	s_mov_b32 m0, s31
	s_nop 0
	global_load_lds_dwordx4 v150, s[24:25]
	s_waitcnt vmcnt(8)
	s_waitcnt lgkmcnt(0)
	s_barrier
	s_waitcnt lgkmcnt(0)
	v_mfma_i32_16x16x64_i8 v[62:65], v[122:125], v[188:191], v[62:65]
	v_mfma_i32_16x16x64_i8 v[58:61], v[130:133], v[188:191], v[58:61]
	v_mfma_i32_16x16x64_i8 v[46:49], v[122:125], v[196:199], v[46:49]
	v_mfma_i32_16x16x64_i8 v[42:45], v[130:133], v[196:199], v[42:45]
	v_mfma_i32_16x16x64_i8 v[30:33], v[122:125], v[204:207], v[30:33]
	v_mfma_i32_16x16x64_i8 v[26:29], v[130:133], v[204:207], v[26:29]
	v_mfma_i32_16x16x64_i8 v[14:17], v[122:125], v[212:215], v[14:17]
	v_mfma_i32_16x16x64_i8 v[10:13], v[130:133], v[212:215], v[10:13]
	v_mfma_i32_16x16x64_i8 v[62:65], v[126:129], v[192:195], v[62:65]
	v_mfma_i32_16x16x64_i8 v[58:61], v[134:137], v[192:195], v[58:61]
	v_mfma_i32_16x16x64_i8 v[46:49], v[126:129], v[200:203], v[46:49]
	v_mfma_i32_16x16x64_i8 v[42:45], v[134:137], v[200:203], v[42:45]
	v_mfma_i32_16x16x64_i8 v[30:33], v[126:129], v[208:211], v[30:33]
	v_mfma_i32_16x16x64_i8 v[26:29], v[134:137], v[208:211], v[26:29]
	v_mfma_i32_16x16x64_i8 v[14:17], v[126:129], v[216:219], v[14:17]
	v_mfma_i32_16x16x64_i8 v[10:13], v[134:137], v[216:219], v[10:13]
	v_mfma_i32_16x16x64_i8 v[54:57], v[172:175], v[188:191], v[54:57]
	v_mfma_i32_16x16x64_i8 v[50:53], v[180:183], v[188:191], v[50:53]
	v_mfma_i32_16x16x64_i8 v[38:41], v[172:175], v[196:199], v[38:41]
	v_mfma_i32_16x16x64_i8 v[34:37], v[180:183], v[196:199], v[34:37]
	v_mfma_i32_16x16x64_i8 v[22:25], v[172:175], v[204:207], v[22:25]
	v_mfma_i32_16x16x64_i8 v[18:21], v[180:183], v[204:207], v[18:21]
	v_mfma_i32_16x16x64_i8 v[6:9], v[172:175], v[212:215], v[6:9]
	v_mfma_i32_16x16x64_i8 v[2:5], v[180:183], v[212:215], v[2:5]
	v_mfma_i32_16x16x64_i8 v[54:57], v[176:179], v[192:195], v[54:57]
	v_mfma_i32_16x16x64_i8 v[50:53], v[184:187], v[192:195], v[50:53]
	v_mfma_i32_16x16x64_i8 v[38:41], v[176:179], v[200:203], v[38:41]
	v_mfma_i32_16x16x64_i8 v[34:37], v[184:187], v[200:203], v[34:37]
	v_mfma_i32_16x16x64_i8 v[22:25], v[176:179], v[208:211], v[22:25]
	v_mfma_i32_16x16x64_i8 v[18:21], v[184:187], v[208:211], v[18:21]
	v_mfma_i32_16x16x64_i8 v[6:9], v[176:179], v[216:219], v[6:9]
	v_mfma_i32_16x16x64_i8 v[2:5], v[184:187], v[216:219], v[2:5]
	s_barrier
	s_add_i32 s38, 0, 0x18000
	s_add_i32 s39, 0, 0x1c000
	v_add_u32_e32 v134, s38, v167
	v_add_u32_e32 v154, s39, v167
	ds_read_b128 v[122:125], v134
	ds_read_b128 v[126:129], v134 offset:1024
	ds_read_b128 v[130:133], v134 offset:2048
	ds_read_b128 v[134:137], v134 offset:3072
	ds_read_b128 v[172:175], v154
	ds_read_b128 v[176:179], v154 offset:1024
	ds_read_b128 v[180:183], v154 offset:2048
	ds_read_b128 v[184:187], v154 offset:3072
	s_add_u32 s24, s24, 0x158000
	s_addc_u32 s25, s25, 0
	s_mov_b32 m0, s33
	ds_read_b128 v[188:191], v171 offset:32768
	ds_read_b128 v[192:195], v171 offset:33792
	ds_read_b128 v[196:199], v171 offset:34816
	ds_read_b128 v[200:203], v171 offset:35840
	ds_read_b128 v[204:207], v171 offset:36864
	ds_read_b128 v[208:211], v171 offset:37888
	ds_read_b128 v[212:215], v171 offset:38912
	ds_read_b128 v[216:219], v171 offset:39936
	global_load_lds_dwordx4 v146, s[24:25]
	s_mov_b32 m0, s34
	s_nop 0
	global_load_lds_dwordx4 v150, s[24:25]
	s_waitcnt vmcnt(8)
	s_waitcnt lgkmcnt(0)
	s_barrier
	s_waitcnt lgkmcnt(0)
	v_mfma_i32_16x16x64_i8 v[142:145], v[122:125], v[188:191], v[142:145]
	v_mfma_i32_16x16x64_i8 v[138:141], v[130:133], v[188:191], v[138:141]
	v_mfma_i32_16x16x64_i8 v[110:113], v[122:125], v[196:199], v[110:113]
	v_mfma_i32_16x16x64_i8 v[106:109], v[130:133], v[196:199], v[106:109]
	v_mfma_i32_16x16x64_i8 v[94:97], v[122:125], v[204:207], v[94:97]
	v_mfma_i32_16x16x64_i8 v[90:93], v[130:133], v[204:207], v[90:93]
	v_mfma_i32_16x16x64_i8 v[78:81], v[122:125], v[212:215], v[78:81]
	v_mfma_i32_16x16x64_i8 v[74:77], v[130:133], v[212:215], v[74:77]
	v_mfma_i32_16x16x64_i8 v[142:145], v[126:129], v[192:195], v[142:145]
	v_mfma_i32_16x16x64_i8 v[138:141], v[134:137], v[192:195], v[138:141]
	v_mfma_i32_16x16x64_i8 v[110:113], v[126:129], v[200:203], v[110:113]
	v_mfma_i32_16x16x64_i8 v[106:109], v[134:137], v[200:203], v[106:109]
	v_mfma_i32_16x16x64_i8 v[94:97], v[126:129], v[208:211], v[94:97]
	v_mfma_i32_16x16x64_i8 v[90:93], v[134:137], v[208:211], v[90:93]
	v_mfma_i32_16x16x64_i8 v[78:81], v[126:129], v[216:219], v[78:81]
	v_mfma_i32_16x16x64_i8 v[74:77], v[134:137], v[216:219], v[74:77]
	v_mfma_i32_16x16x64_i8 v[118:121], v[172:175], v[188:191], v[118:121]
	v_mfma_i32_16x16x64_i8 v[114:117], v[180:183], v[188:191], v[114:117]
	v_mfma_i32_16x16x64_i8 v[102:105], v[172:175], v[196:199], v[102:105]
	v_mfma_i32_16x16x64_i8 v[98:101], v[180:183], v[196:199], v[98:101]
	v_mfma_i32_16x16x64_i8 v[86:89], v[172:175], v[204:207], v[86:89]
	v_mfma_i32_16x16x64_i8 v[82:85], v[180:183], v[204:207], v[82:85]
	v_mfma_i32_16x16x64_i8 v[70:73], v[172:175], v[212:215], v[70:73]
	v_mfma_i32_16x16x64_i8 v[66:69], v[180:183], v[212:215], v[66:69]
	v_mfma_i32_16x16x64_i8 v[118:121], v[176:179], v[192:195], v[118:121]
	v_mfma_i32_16x16x64_i8 v[114:117], v[184:187], v[192:195], v[114:117]
	v_mfma_i32_16x16x64_i8 v[102:105], v[176:179], v[200:203], v[102:105]
	v_mfma_i32_16x16x64_i8 v[98:101], v[184:187], v[200:203], v[98:101]
	v_mfma_i32_16x16x64_i8 v[86:89], v[176:179], v[208:211], v[86:89]
	v_mfma_i32_16x16x64_i8 v[82:85], v[184:187], v[208:211], v[82:85]
	v_mfma_i32_16x16x64_i8 v[70:73], v[176:179], v[216:219], v[70:73]
	v_mfma_i32_16x16x64_i8 v[66:69], v[184:187], v[216:219], v[66:69]
	s_barrier
	s_add_i32 s24, s38, s29
	s_mov_b32 m0, s24
	ds_read_b128 v[188:191], v171 offset:49152
	ds_read_b128 v[192:195], v171 offset:50176
	ds_read_b128 v[196:199], v171 offset:51200
	ds_read_b128 v[200:203], v171 offset:52224
	ds_read_b128 v[204:207], v171 offset:53248
	ds_read_b128 v[208:211], v171 offset:54272
	ds_read_b128 v[212:215], v171 offset:55296
	ds_read_b128 v[216:219], v171 offset:56320
	global_load_lds_dwordx4 v148, s[98:99]
	s_add_i32 m0, s24, 0x2000
	s_add_u32 s22, s22, 0x158080
	s_addc_u32 s23, s23, 0
	s_add_i32 s24, s39, s29
	global_load_lds_dwordx4 v152, s[98:99]
	s_mov_b32 m0, s24
	s_nop 0
	global_load_lds_dwordx4 v148, s[22:23]
	s_add_i32 m0, s24, 0x2000
	s_nop 0
	global_load_lds_dwordx4 v152, s[22:23]
	s_mov_b32 m0, s36
	s_nop 0
	global_load_lds_dwordx4 v146, s[100:101]
	s_mov_b32 m0, s37
	s_nop 0
	global_load_lds_dwordx4 v150, s[100:101]
	s_waitcnt vmcnt(8)
	s_waitcnt lgkmcnt(0)
	s_barrier
	s_waitcnt lgkmcnt(0)
	v_mfma_i32_16x16x64_i8 v[62:65], v[122:125], v[188:191], v[62:65]
	v_mfma_i32_16x16x64_i8 v[58:61], v[130:133], v[188:191], v[58:61]
	v_mfma_i32_16x16x64_i8 v[46:49], v[122:125], v[196:199], v[46:49]
	v_mfma_i32_16x16x64_i8 v[42:45], v[130:133], v[196:199], v[42:45]
	v_mfma_i32_16x16x64_i8 v[30:33], v[122:125], v[204:207], v[30:33]
	v_mfma_i32_16x16x64_i8 v[26:29], v[130:133], v[204:207], v[26:29]
	v_mfma_i32_16x16x64_i8 v[14:17], v[122:125], v[212:215], v[14:17]
	v_mfma_i32_16x16x64_i8 v[10:13], v[130:133], v[212:215], v[10:13]
	v_mfma_i32_16x16x64_i8 v[62:65], v[126:129], v[192:195], v[62:65]
	v_mfma_i32_16x16x64_i8 v[58:61], v[134:137], v[192:195], v[58:61]
	v_mfma_i32_16x16x64_i8 v[46:49], v[126:129], v[200:203], v[46:49]
	v_mfma_i32_16x16x64_i8 v[42:45], v[134:137], v[200:203], v[42:45]
	v_mfma_i32_16x16x64_i8 v[30:33], v[126:129], v[208:211], v[30:33]
	v_mfma_i32_16x16x64_i8 v[26:29], v[134:137], v[208:211], v[26:29]
	v_mfma_i32_16x16x64_i8 v[14:17], v[126:129], v[216:219], v[14:17]
	v_mfma_i32_16x16x64_i8 v[10:13], v[134:137], v[216:219], v[10:13]
	v_mfma_i32_16x16x64_i8 v[54:57], v[172:175], v[188:191], v[54:57]
	v_mfma_i32_16x16x64_i8 v[50:53], v[180:183], v[188:191], v[50:53]
	v_mfma_i32_16x16x64_i8 v[38:41], v[172:175], v[196:199], v[38:41]
	v_mfma_i32_16x16x64_i8 v[34:37], v[180:183], v[196:199], v[34:37]
	v_mfma_i32_16x16x64_i8 v[22:25], v[172:175], v[204:207], v[22:25]
	v_mfma_i32_16x16x64_i8 v[18:21], v[180:183], v[204:207], v[18:21]
	v_mfma_i32_16x16x64_i8 v[6:9], v[172:175], v[212:215], v[6:9]
	v_mfma_i32_16x16x64_i8 v[2:5], v[180:183], v[212:215], v[2:5]
	v_mfma_i32_16x16x64_i8 v[54:57], v[176:179], v[192:195], v[54:57]
	v_mfma_i32_16x16x64_i8 v[50:53], v[184:187], v[192:195], v[50:53]
	v_mfma_i32_16x16x64_i8 v[38:41], v[176:179], v[200:203], v[38:41]
	v_mfma_i32_16x16x64_i8 v[34:37], v[184:187], v[200:203], v[34:37]
	v_mfma_i32_16x16x64_i8 v[22:25], v[176:179], v[208:211], v[22:25]
	v_mfma_i32_16x16x64_i8 v[18:21], v[184:187], v[208:211], v[18:21]
	v_mfma_i32_16x16x64_i8 v[6:9], v[176:179], v[216:219], v[6:9]
	v_mfma_i32_16x16x64_i8 v[2:5], v[184:187], v[216:219], v[2:5]
	s_barrier
	s_add_i32 s49, s49, 2
	s_add_u32 s20, s20, 0x100
	s_addc_u32 s21, s21, 0
	s_add_u32 s47, s47, 0x100
	s_addc_u32 s48, s48, 0
	s_cmpk_gt_u32 s49, 0x53
	s_cbranch_scc0 .LBB0_1899
	s_and_b64 vcc, exec, s[16:17]
	s_cbranch_vccz .LBB0_1902
	s_barrier

.LBB0_1960:
	s_setprio 0
	s_cmp_lt_i32 s70, 12
	s_cselect_b64 s[0:1], -1, 0
	s_and_b64 s[0:1], s[0:1], s[2:3]
	s_andn2_b64 vcc, exec, s[0:1]
	s_cbranch_vccnz .LBB0_1966
	v_readlane_b32 s0, v254, 51
	v_readlane_b32 s8, v254, 59
	v_readlane_b32 s1, v254, 52
	v_readlane_b32 s2, v254, 53
	v_readlane_b32 s3, v254, 54
	v_readlane_b32 s4, v254, 55
	v_readlane_b32 s9, v254, 60
	s_add_u32 s0, s8, 0xc000
	s_addc_u32 s1, s9, 0
	v_lshl_add_u32 v1, v0, 4, 0
	s_mov_b64 s[2:3], 0
	v_mov_b32_e32 v3, 0
	s_movk_i32 s4, 0x5ff
	v_readlane_b32 s5, v254, 56
	v_readlane_b32 s6, v254, 57
	v_readlane_b32 s7, v254, 58
	v_readlane_b32 s10, v254, 61
	v_readlane_b32 s11, v254, 62
	v_readlane_b32 s12, v254, 63
	v_readlane_b32 s13, v255, 0
	v_readlane_b32 s14, v255, 1
	v_readlane_b32 s15, v255, 2
